# hyena third filter layer fully unrolled with four weight register sets, weight loads three steps ahead
# baseline (speedup 1.0000x reference)
;     ...
;         for (int k4 = 0; k4 < 16; ++k4) {
;             float wf[4], wb[4];
; #pragma unroll
;             for (int j = 0; j < 4; ++j) { wf[j] = w3[(k4 * 4 + j) * 1024 + tid]; wb[j] = w3[(k4 * 4 + j) * 1024 + 512 + tid]; }
; #pragma unroll
;             for (int pp = 0; pp < 16; ++pp) {
;                 const float4 hv = *(const float4*)&h2[(hp * 16 + pp) * 64 + k4 * 4];
;                 accf[pp] += hv.x * wf[0]; accf[pp] += hv.y * wf[1]; accf[pp] += hv.z * wf[2]; accf[pp] += hv.w * wf[3];
;                 accb[pp] += hv.x * wb[0]; accb[pp] += hv.y * wb[1]; accb[pp] += hv.z * wb[2]; accb[pp] += hv.w * wb[3];
;             }
;         }
.LBB0_76:
	v_lshlrev_b32_e32 v62, 2, v0
	v_readlane_b32 s98, v253, 59
	v_readlane_b32 s99, v253, 60
	s_mov_b32 s101, s2
	global_load_dword v204, v62, s[98:99]
	global_load_dword v208, v62, s[98:99] offset:2048
	s_add_u32 s98, s98, 0x1000
	s_addc_u32 s99, s99, 0
	global_load_dword v205, v62, s[98:99]
	global_load_dword v209, v62, s[98:99] offset:2048
	s_add_u32 s98, s98, 0x1000
	s_addc_u32 s99, s99, 0
	global_load_dword v206, v62, s[98:99]
	global_load_dword v210, v62, s[98:99] offset:2048
	s_add_u32 s98, s98, 0x1000
	s_addc_u32 s99, s99, 0
	global_load_dword v207, v62, s[98:99]
	global_load_dword v211, v62, s[98:99] offset:2048
	s_add_u32 s98, s98, 0x1000
	s_addc_u32 s99, s99, 0
	global_load_dword v212, v62, s[98:99]
	global_load_dword v216, v62, s[98:99] offset:2048
	s_add_u32 s98, s98, 0x1000
	s_addc_u32 s99, s99, 0
	global_load_dword v213, v62, s[98:99]
	global_load_dword v217, v62, s[98:99] offset:2048
	s_add_u32 s98, s98, 0x1000
	s_addc_u32 s99, s99, 0
	global_load_dword v214, v62, s[98:99]
	global_load_dword v218, v62, s[98:99] offset:2048
	s_add_u32 s98, s98, 0x1000
	s_addc_u32 s99, s99, 0
	global_load_dword v215, v62, s[98:99]
	global_load_dword v219, v62, s[98:99] offset:2048
	s_add_u32 s98, s98, 0x1000
	s_addc_u32 s99, s99, 0
	global_load_dword v220, v62, s[98:99]
	global_load_dword v224, v62, s[98:99] offset:2048
	s_add_u32 s98, s98, 0x1000
	s_addc_u32 s99, s99, 0
	global_load_dword v221, v62, s[98:99]
	global_load_dword v225, v62, s[98:99] offset:2048
	s_add_u32 s98, s98, 0x1000
	s_addc_u32 s99, s99, 0
	global_load_dword v222, v62, s[98:99]
	global_load_dword v226, v62, s[98:99] offset:2048
	s_add_u32 s98, s98, 0x1000
	s_addc_u32 s99, s99, 0
	global_load_dword v223, v62, s[98:99]
	global_load_dword v227, v62, s[98:99] offset:2048
	s_add_u32 s98, s98, 0x1000
	s_addc_u32 s99, s99, 0
	global_load_dword v228, v62, s[98:99]
	global_load_dword v232, v62, s[98:99] offset:2048
	s_add_u32 s98, s98, 0x1000
	s_addc_u32 s99, s99, 0
	global_load_dword v229, v62, s[98:99]
	global_load_dword v233, v62, s[98:99] offset:2048
	s_add_u32 s98, s98, 0x1000
	s_addc_u32 s99, s99, 0
	global_load_dword v230, v62, s[98:99]
	global_load_dword v234, v62, s[98:99] offset:2048
	s_add_u32 s98, s98, 0x1000
	s_addc_u32 s99, s99, 0
	global_load_dword v231, v62, s[98:99]
	global_load_dword v235, v62, s[98:99] offset:2048
	s_add_u32 s98, s98, 0x1000
	s_addc_u32 s99, s99, 0
	v_mov_b32_e32 v63, s101
	s_add_i32 s101, s101, 16
	ds_read_b128 v[94:97], v63
	ds_read_b128 v[98:101], v63 offset:256
	s_waitcnt vmcnt(24)
	ds_read_b128 v[58:61], v63 offset:512
	s_waitcnt lgkmcnt(2)
	v_fmac_f32_e32 v54, v204, v94
	v_fmac_f32_e32 v56, v208, v94
	v_fmac_f32_e32 v54, v205, v95
	v_fmac_f32_e32 v56, v209, v95
	v_fmac_f32_e32 v54, v206, v96
	v_fmac_f32_e32 v56, v210, v96
	v_fmac_f32_e32 v54, v207, v97
	v_fmac_f32_e32 v56, v211, v97
	ds_read_b128 v[94:97], v63 offset:768
	s_waitcnt lgkmcnt(2)
	v_fmac_f32_e32 v55, v204, v98
	v_fmac_f32_e32 v57, v208, v98
	v_fmac_f32_e32 v55, v205, v99
	v_fmac_f32_e32 v57, v209, v99
	v_fmac_f32_e32 v55, v206, v100
	v_fmac_f32_e32 v57, v210, v100
	v_fmac_f32_e32 v55, v207, v101
	v_fmac_f32_e32 v57, v211, v101
	ds_read_b128 v[98:101], v63 offset:1024
	s_waitcnt lgkmcnt(2)
	v_fmac_f32_e32 v50, v204, v58
	v_fmac_f32_e32 v52, v208, v58
	v_fmac_f32_e32 v50, v205, v59
	v_fmac_f32_e32 v52, v209, v59
	v_fmac_f32_e32 v50, v206, v60
	v_fmac_f32_e32 v52, v210, v60
	v_fmac_f32_e32 v50, v207, v61
	v_fmac_f32_e32 v52, v211, v61
	ds_read_b128 v[58:61], v63 offset:1280
	s_waitcnt lgkmcnt(2)
	v_fmac_f32_e32 v51, v204, v94
	v_fmac_f32_e32 v53, v208, v94
	v_fmac_f32_e32 v51, v205, v95
	v_fmac_f32_e32 v53, v209, v95
	v_fmac_f32_e32 v51, v206, v96
	v_fmac_f32_e32 v53, v210, v96
	v_fmac_f32_e32 v51, v207, v97
	v_fmac_f32_e32 v53, v211, v97
	ds_read_b128 v[94:97], v63 offset:1536
	s_waitcnt lgkmcnt(2)
	v_fmac_f32_e32 v46, v204, v98
	v_fmac_f32_e32 v48, v208, v98
	v_fmac_f32_e32 v46, v205, v99
	v_fmac_f32_e32 v48, v209, v99
	v_fmac_f32_e32 v46, v206, v100
	v_fmac_f32_e32 v48, v210, v100
	v_fmac_f32_e32 v46, v207, v101
	v_fmac_f32_e32 v48, v211, v101
	ds_read_b128 v[98:101], v63 offset:1792
	s_waitcnt lgkmcnt(2)
	v_fmac_f32_e32 v47, v204, v58
	v_fmac_f32_e32 v49, v208, v58
	v_fmac_f32_e32 v47, v205, v59
	v_fmac_f32_e32 v49, v209, v59
	v_fmac_f32_e32 v47, v206, v60
	v_fmac_f32_e32 v49, v210, v60
	v_fmac_f32_e32 v47, v207, v61
	v_fmac_f32_e32 v49, v211, v61
	ds_read_b128 v[58:61], v63 offset:2048
	s_waitcnt lgkmcnt(2)
	v_fmac_f32_e32 v42, v204, v94
	v_fmac_f32_e32 v44, v208, v94
	v_fmac_f32_e32 v42, v205, v95
	v_fmac_f32_e32 v44, v209, v95
	v_fmac_f32_e32 v42, v206, v96
	v_fmac_f32_e32 v44, v210, v96
	v_fmac_f32_e32 v42, v207, v97
	v_fmac_f32_e32 v44, v211, v97
	ds_read_b128 v[94:97], v63 offset:2304
	s_waitcnt lgkmcnt(2)
	v_fmac_f32_e32 v43, v204, v98
	v_fmac_f32_e32 v45, v208, v98
	v_fmac_f32_e32 v43, v205, v99
	v_fmac_f32_e32 v45, v209, v99
	v_fmac_f32_e32 v43, v206, v100
	v_fmac_f32_e32 v45, v210, v100
	v_fmac_f32_e32 v43, v207, v101
	v_fmac_f32_e32 v45, v211, v101
	ds_read_b128 v[98:101], v63 offset:2560
	s_waitcnt lgkmcnt(2)
	v_fmac_f32_e32 v38, v204, v58
	v_fmac_f32_e32 v40, v208, v58
	v_fmac_f32_e32 v38, v205, v59
	v_fmac_f32_e32 v40, v209, v59
	v_fmac_f32_e32 v38, v206, v60
	v_fmac_f32_e32 v40, v210, v60
	v_fmac_f32_e32 v38, v207, v61
	v_fmac_f32_e32 v40, v211, v61
	ds_read_b128 v[58:61], v63 offset:2816
	s_waitcnt lgkmcnt(2)
	v_fmac_f32_e32 v39, v204, v94
	v_fmac_f32_e32 v41, v208, v94
	v_fmac_f32_e32 v39, v205, v95
	v_fmac_f32_e32 v41, v209, v95
	v_fmac_f32_e32 v39, v206, v96
	v_fmac_f32_e32 v41, v210, v96
	v_fmac_f32_e32 v39, v207, v97
	v_fmac_f32_e32 v41, v211, v97
	ds_read_b128 v[94:97], v63 offset:3072
	s_waitcnt lgkmcnt(2)
;     ...
;         for (int k4 = 0; k4 < 16; ++k4) {
;             float wf[4], wb[4];
; #pragma unroll
;             for (int j = 0; j < 4; ++j) { wf[j] = w3[(k4 * 4 + j) * 1024 + tid]; wb[j] = w3[(k4 * 4 + j) * 1024 + 512 + tid]; }
; #pragma unroll
;             for (int pp = 0; pp < 16; ++pp) {
;                 const float4 hv = *(const float4*)&h2[(hp * 16 + pp) * 64 + k4 * 4];
;                 accf[pp] += hv.x * wf[0]; accf[pp] += hv.y * wf[1]; accf[pp] += hv.z * wf[2]; accf[pp] += hv.w * wf[3];
;                 accb[pp] += hv.x * wb[0]; accb[pp] += hv.y * wb[1]; accb[pp] += hv.z * wb[2]; accb[pp] += hv.w * wb[3];
;             }
;         }
	v_fmac_f32_e32 v34, v204, v98
	v_fmac_f32_e32 v36, v208, v98
	v_fmac_f32_e32 v34, v205, v99
	v_fmac_f32_e32 v36, v209, v99
	v_fmac_f32_e32 v34, v206, v100
	v_fmac_f32_e32 v36, v210, v100
	v_fmac_f32_e32 v34, v207, v101
	v_fmac_f32_e32 v36, v211, v101
	ds_read_b128 v[98:101], v63 offset:3328
	s_waitcnt lgkmcnt(2)
	v_fmac_f32_e32 v35, v204, v58
	v_fmac_f32_e32 v37, v208, v58
	v_fmac_f32_e32 v35, v205, v59
	v_fmac_f32_e32 v37, v209, v59
	v_fmac_f32_e32 v35, v206, v60
	v_fmac_f32_e32 v37, v210, v60
	v_fmac_f32_e32 v35, v207, v61
	v_fmac_f32_e32 v37, v211, v61
	ds_read_b128 v[58:61], v63 offset:3584
	s_waitcnt lgkmcnt(2)
	v_fmac_f32_e32 v30, v204, v94
	v_fmac_f32_e32 v32, v208, v94
	v_fmac_f32_e32 v30, v205, v95
	v_fmac_f32_e32 v32, v209, v95
	v_fmac_f32_e32 v30, v206, v96
	v_fmac_f32_e32 v32, v210, v96
	v_fmac_f32_e32 v30, v207, v97
	v_fmac_f32_e32 v32, v211, v97
	ds_read_b128 v[94:97], v63 offset:3840
	s_waitcnt lgkmcnt(2)
	v_fmac_f32_e32 v31, v204, v98
	v_fmac_f32_e32 v33, v208, v98
	v_fmac_f32_e32 v31, v205, v99
	v_fmac_f32_e32 v33, v209, v99
	v_fmac_f32_e32 v31, v206, v100
	v_fmac_f32_e32 v33, v210, v100
	v_fmac_f32_e32 v31, v207, v101
	v_fmac_f32_e32 v33, v211, v101
	s_waitcnt lgkmcnt(1)
	v_fmac_f32_e32 v26, v204, v58
	v_fmac_f32_e32 v28, v208, v58
	v_fmac_f32_e32 v26, v205, v59
	v_fmac_f32_e32 v28, v209, v59
	v_fmac_f32_e32 v26, v206, v60
	v_fmac_f32_e32 v28, v210, v60
	v_fmac_f32_e32 v26, v207, v61
	v_fmac_f32_e32 v28, v211, v61
	s_waitcnt lgkmcnt(0)
	v_fmac_f32_e32 v27, v204, v94
	v_fmac_f32_e32 v29, v208, v94
	v_fmac_f32_e32 v27, v205, v95
	v_fmac_f32_e32 v29, v209, v95
	v_fmac_f32_e32 v27, v206, v96
	v_fmac_f32_e32 v29, v210, v96
	v_fmac_f32_e32 v27, v207, v97
	v_fmac_f32_e32 v29, v211, v97
	global_load_dword v204, v62, s[98:99]
	global_load_dword v208, v62, s[98:99] offset:2048
	s_add_u32 s98, s98, 0x1000
	s_addc_u32 s99, s99, 0
	global_load_dword v205, v62, s[98:99]
	global_load_dword v209, v62, s[98:99] offset:2048
	s_add_u32 s98, s98, 0x1000
	s_addc_u32 s99, s99, 0
	global_load_dword v206, v62, s[98:99]
	global_load_dword v210, v62, s[98:99] offset:2048
	s_add_u32 s98, s98, 0x1000
	s_addc_u32 s99, s99, 0
	global_load_dword v207, v62, s[98:99]
	global_load_dword v211, v62, s[98:99] offset:2048
	s_add_u32 s98, s98, 0x1000
	s_addc_u32 s99, s99, 0
	v_mov_b32_e32 v63, s101
	s_add_i32 s101, s101, 16
	ds_read_b128 v[94:97], v63
	ds_read_b128 v[98:101], v63 offset:256
	s_waitcnt vmcnt(24)
	ds_read_b128 v[58:61], v63 offset:512
	s_waitcnt lgkmcnt(2)
	v_fmac_f32_e32 v54, v212, v94
	v_fmac_f32_e32 v56, v216, v94
	v_fmac_f32_e32 v54, v213, v95
	v_fmac_f32_e32 v56, v217, v95
	v_fmac_f32_e32 v54, v214, v96
	v_fmac_f32_e32 v56, v218, v96
	v_fmac_f32_e32 v54, v215, v97
	v_fmac_f32_e32 v56, v219, v97
	ds_read_b128 v[94:97], v63 offset:768
	s_waitcnt lgkmcnt(2)
	v_fmac_f32_e32 v55, v212, v98
	v_fmac_f32_e32 v57, v216, v98
	v_fmac_f32_e32 v55, v213, v99
	v_fmac_f32_e32 v57, v217, v99
	v_fmac_f32_e32 v55, v214, v100
	v_fmac_f32_e32 v57, v218, v100
	v_fmac_f32_e32 v55, v215, v101
	v_fmac_f32_e32 v57, v219, v101
	ds_read_b128 v[98:101], v63 offset:1024
	s_waitcnt lgkmcnt(2)
	v_fmac_f32_e32 v50, v212, v58
	v_fmac_f32_e32 v52, v216, v58
	v_fmac_f32_e32 v50, v213, v59
	v_fmac_f32_e32 v52, v217, v59
	v_fmac_f32_e32 v50, v214, v60
	v_fmac_f32_e32 v52, v218, v60
	v_fmac_f32_e32 v50, v215, v61
	v_fmac_f32_e32 v52, v219, v61
	ds_read_b128 v[58:61], v63 offset:1280
	s_waitcnt lgkmcnt(2)
	v_fmac_f32_e32 v51, v212, v94
	v_fmac_f32_e32 v53, v216, v94
	v_fmac_f32_e32 v51, v213, v95
	v_fmac_f32_e32 v53, v217, v95
	v_fmac_f32_e32 v51, v214, v96
	v_fmac_f32_e32 v53, v218, v96
	v_fmac_f32_e32 v51, v215, v97
	v_fmac_f32_e32 v53, v219, v97
	ds_read_b128 v[94:97], v63 offset:1536
	s_waitcnt lgkmcnt(2)
	v_fmac_f32_e32 v46, v212, v98
	v_fmac_f32_e32 v48, v216, v98
	v_fmac_f32_e32 v46, v213, v99
	v_fmac_f32_e32 v48, v217, v99
	v_fmac_f32_e32 v46, v214, v100
	v_fmac_f32_e32 v48, v218, v100
	v_fmac_f32_e32 v46, v215, v101
	v_fmac_f32_e32 v48, v219, v101
	ds_read_b128 v[98:101], v63 offset:1792
	s_waitcnt lgkmcnt(2)
	v_fmac_f32_e32 v47, v212, v58
	v_fmac_f32_e32 v49, v216, v58
	v_fmac_f32_e32 v47, v213, v59
	v_fmac_f32_e32 v49, v217, v59
	v_fmac_f32_e32 v47, v214, v60
	v_fmac_f32_e32 v49, v218, v60
	v_fmac_f32_e32 v47, v215, v61
	v_fmac_f32_e32 v49, v219, v61
	ds_read_b128 v[58:61], v63 offset:2048
	s_waitcnt lgkmcnt(2)
	v_fmac_f32_e32 v42, v212, v94
	v_fmac_f32_e32 v44, v216, v94
	v_fmac_f32_e32 v42, v213, v95
	v_fmac_f32_e32 v44, v217, v95
	v_fmac_f32_e32 v42, v214, v96
	v_fmac_f32_e32 v44, v218, v96
	v_fmac_f32_e32 v42, v215, v97
	v_fmac_f32_e32 v44, v219, v97
	ds_read_b128 v[94:97], v63 offset:2304
	s_waitcnt lgkmcnt(2)
	v_fmac_f32_e32 v43, v212, v98
	v_fmac_f32_e32 v45, v216, v98
	v_fmac_f32_e32 v43, v213, v99
	v_fmac_f32_e32 v45, v217, v99
	v_fmac_f32_e32 v43, v214, v100
	v_fmac_f32_e32 v45, v218, v100
	v_fmac_f32_e32 v43, v215, v101
	v_fmac_f32_e32 v45, v219, v101
	ds_read_b128 v[98:101], v63 offset:2560
	s_waitcnt lgkmcnt(2)
	v_fmac_f32_e32 v38, v212, v58
	v_fmac_f32_e32 v40, v216, v58
	v_fmac_f32_e32 v38, v213, v59
	v_fmac_f32_e32 v40, v217, v59
	v_fmac_f32_e32 v38, v214, v60
	v_fmac_f32_e32 v40, v218, v60
	v_fmac_f32_e32 v38, v215, v61
	v_fmac_f32_e32 v40, v219, v61
	ds_read_b128 v[58:61], v63 offset:2816
	s_waitcnt lgkmcnt(2)
	v_fmac_f32_e32 v39, v212, v94
	v_fmac_f32_e32 v41, v216, v94
	v_fmac_f32_e32 v39, v213, v95
	v_fmac_f32_e32 v41, v217, v95
	v_fmac_f32_e32 v39, v214, v96
	v_fmac_f32_e32 v41, v218, v96
	v_fmac_f32_e32 v39, v215, v97
	v_fmac_f32_e32 v41, v219, v97
	ds_read_b128 v[94:97], v63 offset:3072
	s_waitcnt lgkmcnt(2)
;     ...
;         for (int k4 = 0; k4 < 16; ++k4) {
;             float wf[4], wb[4];
; #pragma unroll
;             for (int j = 0; j < 4; ++j) { wf[j] = w3[(k4 * 4 + j) * 1024 + tid]; wb[j] = w3[(k4 * 4 + j) * 1024 + 512 + tid]; }
; #pragma unroll
;             for (int pp = 0; pp < 16; ++pp) {
;                 const float4 hv = *(const float4*)&h2[(hp * 16 + pp) * 64 + k4 * 4];
;                 accf[pp] += hv.x * wf[0]; accf[pp] += hv.y * wf[1]; accf[pp] += hv.z * wf[2]; accf[pp] += hv.w * wf[3];
;                 accb[pp] += hv.x * wb[0]; accb[pp] += hv.y * wb[1]; accb[pp] += hv.z * wb[2]; accb[pp] += hv.w * wb[3];
;             }
;         }
	v_fmac_f32_e32 v34, v212, v98
	v_fmac_f32_e32 v36, v216, v98
	v_fmac_f32_e32 v34, v213, v99
	v_fmac_f32_e32 v36, v217, v99
	v_fmac_f32_e32 v34, v214, v100
	v_fmac_f32_e32 v36, v218, v100
	v_fmac_f32_e32 v34, v215, v101
	v_fmac_f32_e32 v36, v219, v101
	ds_read_b128 v[98:101], v63 offset:3328
	s_waitcnt lgkmcnt(2)
	v_fmac_f32_e32 v35, v212, v58
	v_fmac_f32_e32 v37, v216, v58
	v_fmac_f32_e32 v35, v213, v59
	v_fmac_f32_e32 v37, v217, v59
	v_fmac_f32_e32 v35, v214, v60
	v_fmac_f32_e32 v37, v218, v60
	v_fmac_f32_e32 v35, v215, v61
	v_fmac_f32_e32 v37, v219, v61
	ds_read_b128 v[58:61], v63 offset:3584
	s_waitcnt lgkmcnt(2)
	v_fmac_f32_e32 v30, v212, v94
	v_fmac_f32_e32 v32, v216, v94
	v_fmac_f32_e32 v30, v213, v95
	v_fmac_f32_e32 v32, v217, v95
	v_fmac_f32_e32 v30, v214, v96
	v_fmac_f32_e32 v32, v218, v96
	v_fmac_f32_e32 v30, v215, v97
	v_fmac_f32_e32 v32, v219, v97
	ds_read_b128 v[94:97], v63 offset:3840
	s_waitcnt lgkmcnt(2)
	v_fmac_f32_e32 v31, v212, v98
	v_fmac_f32_e32 v33, v216, v98
	v_fmac_f32_e32 v31, v213, v99
	v_fmac_f32_e32 v33, v217, v99
	v_fmac_f32_e32 v31, v214, v100
	v_fmac_f32_e32 v33, v218, v100
	v_fmac_f32_e32 v31, v215, v101
	v_fmac_f32_e32 v33, v219, v101
	s_waitcnt lgkmcnt(1)
	v_fmac_f32_e32 v26, v212, v58
	v_fmac_f32_e32 v28, v216, v58
	v_fmac_f32_e32 v26, v213, v59
	v_fmac_f32_e32 v28, v217, v59
	v_fmac_f32_e32 v26, v214, v60
	v_fmac_f32_e32 v28, v218, v60
	v_fmac_f32_e32 v26, v215, v61
	v_fmac_f32_e32 v28, v219, v61
	s_waitcnt lgkmcnt(0)
	v_fmac_f32_e32 v27, v212, v94
	v_fmac_f32_e32 v29, v216, v94
	v_fmac_f32_e32 v27, v213, v95
	v_fmac_f32_e32 v29, v217, v95
	v_fmac_f32_e32 v27, v214, v96
	v_fmac_f32_e32 v29, v218, v96
	v_fmac_f32_e32 v27, v215, v97
	v_fmac_f32_e32 v29, v219, v97
	global_load_dword v212, v62, s[98:99]
	global_load_dword v216, v62, s[98:99] offset:2048
	s_add_u32 s98, s98, 0x1000
	s_addc_u32 s99, s99, 0
	global_load_dword v213, v62, s[98:99]
	global_load_dword v217, v62, s[98:99] offset:2048
	s_add_u32 s98, s98, 0x1000
	s_addc_u32 s99, s99, 0
	global_load_dword v214, v62, s[98:99]
	global_load_dword v218, v62, s[98:99] offset:2048
	s_add_u32 s98, s98, 0x1000
	s_addc_u32 s99, s99, 0
	global_load_dword v215, v62, s[98:99]
	global_load_dword v219, v62, s[98:99] offset:2048
	s_add_u32 s98, s98, 0x1000
	s_addc_u32 s99, s99, 0
	v_mov_b32_e32 v63, s101
	s_add_i32 s101, s101, 16
	ds_read_b128 v[94:97], v63
	ds_read_b128 v[98:101], v63 offset:256
	s_waitcnt vmcnt(24)
	ds_read_b128 v[58:61], v63 offset:512
	s_waitcnt lgkmcnt(2)
	v_fmac_f32_e32 v54, v220, v94
	v_fmac_f32_e32 v56, v224, v94
	v_fmac_f32_e32 v54, v221, v95
	v_fmac_f32_e32 v56, v225, v95
	v_fmac_f32_e32 v54, v222, v96
	v_fmac_f32_e32 v56, v226, v96
	v_fmac_f32_e32 v54, v223, v97
	v_fmac_f32_e32 v56, v227, v97
	ds_read_b128 v[94:97], v63 offset:768
	s_waitcnt lgkmcnt(2)
	v_fmac_f32_e32 v55, v220, v98
	v_fmac_f32_e32 v57, v224, v98
	v_fmac_f32_e32 v55, v221, v99
	v_fmac_f32_e32 v57, v225, v99
	v_fmac_f32_e32 v55, v222, v100
	v_fmac_f32_e32 v57, v226, v100
	v_fmac_f32_e32 v55, v223, v101
	v_fmac_f32_e32 v57, v227, v101
	ds_read_b128 v[98:101], v63 offset:1024
	s_waitcnt lgkmcnt(2)
	v_fmac_f32_e32 v50, v220, v58
	v_fmac_f32_e32 v52, v224, v58
	v_fmac_f32_e32 v50, v221, v59
	v_fmac_f32_e32 v52, v225, v59
	v_fmac_f32_e32 v50, v222, v60
	v_fmac_f32_e32 v52, v226, v60
	v_fmac_f32_e32 v50, v223, v61
	v_fmac_f32_e32 v52, v227, v61
	ds_read_b128 v[58:61], v63 offset:1280
	s_waitcnt lgkmcnt(2)
	v_fmac_f32_e32 v51, v220, v94
	v_fmac_f32_e32 v53, v224, v94
	v_fmac_f32_e32 v51, v221, v95
	v_fmac_f32_e32 v53, v225, v95
	v_fmac_f32_e32 v51, v222, v96
	v_fmac_f32_e32 v53, v226, v96
	v_fmac_f32_e32 v51, v223, v97
	v_fmac_f32_e32 v53, v227, v97
	ds_read_b128 v[94:97], v63 offset:1536
	s_waitcnt lgkmcnt(2)
	v_fmac_f32_e32 v46, v220, v98
	v_fmac_f32_e32 v48, v224, v98
	v_fmac_f32_e32 v46, v221, v99
	v_fmac_f32_e32 v48, v225, v99
	v_fmac_f32_e32 v46, v222, v100
	v_fmac_f32_e32 v48, v226, v100
	v_fmac_f32_e32 v46, v223, v101
	v_fmac_f32_e32 v48, v227, v101
	ds_read_b128 v[98:101], v63 offset:1792
	s_waitcnt lgkmcnt(2)
	v_fmac_f32_e32 v47, v220, v58
	v_fmac_f32_e32 v49, v224, v58
	v_fmac_f32_e32 v47, v221, v59
	v_fmac_f32_e32 v49, v225, v59
	v_fmac_f32_e32 v47, v222, v60
	v_fmac_f32_e32 v49, v226, v60
	v_fmac_f32_e32 v47, v223, v61
	v_fmac_f32_e32 v49, v227, v61
	ds_read_b128 v[58:61], v63 offset:2048
	s_waitcnt lgkmcnt(2)
	v_fmac_f32_e32 v42, v220, v94
	v_fmac_f32_e32 v44, v224, v94
	v_fmac_f32_e32 v42, v221, v95
	v_fmac_f32_e32 v44, v225, v95
	v_fmac_f32_e32 v42, v222, v96
	v_fmac_f32_e32 v44, v226, v96
	v_fmac_f32_e32 v42, v223, v97
	v_fmac_f32_e32 v44, v227, v97
	ds_read_b128 v[94:97], v63 offset:2304
	s_waitcnt lgkmcnt(2)
	v_fmac_f32_e32 v43, v220, v98
	v_fmac_f32_e32 v45, v224, v98
	v_fmac_f32_e32 v43, v221, v99
	v_fmac_f32_e32 v45, v225, v99
	v_fmac_f32_e32 v43, v222, v100
	v_fmac_f32_e32 v45, v226, v100
	v_fmac_f32_e32 v43, v223, v101
	v_fmac_f32_e32 v45, v227, v101
	ds_read_b128 v[98:101], v63 offset:2560
	s_waitcnt lgkmcnt(2)
	v_fmac_f32_e32 v38, v220, v58
	v_fmac_f32_e32 v40, v224, v58
	v_fmac_f32_e32 v38, v221, v59
	v_fmac_f32_e32 v40, v225, v59
	v_fmac_f32_e32 v38, v222, v60
	v_fmac_f32_e32 v40, v226, v60
	v_fmac_f32_e32 v38, v223, v61
	v_fmac_f32_e32 v40, v227, v61
	ds_read_b128 v[58:61], v63 offset:2816
	s_waitcnt lgkmcnt(2)
	v_fmac_f32_e32 v39, v220, v94
	v_fmac_f32_e32 v41, v224, v94
	v_fmac_f32_e32 v39, v221, v95
	v_fmac_f32_e32 v41, v225, v95
	v_fmac_f32_e32 v39, v222, v96
	v_fmac_f32_e32 v41, v226, v96
	v_fmac_f32_e32 v39, v223, v97
	v_fmac_f32_e32 v41, v227, v97
	ds_read_b128 v[94:97], v63 offset:3072
	s_waitcnt lgkmcnt(2)
;     ...
;         for (int k4 = 0; k4 < 16; ++k4) {
;             float wf[4], wb[4];
; #pragma unroll
;             for (int j = 0; j < 4; ++j) { wf[j] = w3[(k4 * 4 + j) * 1024 + tid]; wb[j] = w3[(k4 * 4 + j) * 1024 + 512 + tid]; }
; #pragma unroll
;             for (int pp = 0; pp < 16; ++pp) {
;                 const float4 hv = *(const float4*)&h2[(hp * 16 + pp) * 64 + k4 * 4];
;                 accf[pp] += hv.x * wf[0]; accf[pp] += hv.y * wf[1]; accf[pp] += hv.z * wf[2]; accf[pp] += hv.w * wf[3];
;                 accb[pp] += hv.x * wb[0]; accb[pp] += hv.y * wb[1]; accb[pp] += hv.z * wb[2]; accb[pp] += hv.w * wb[3];
;             }
;         }
	v_fmac_f32_e32 v34, v220, v98
	v_fmac_f32_e32 v36, v224, v98
	v_fmac_f32_e32 v34, v221, v99
	v_fmac_f32_e32 v36, v225, v99
	v_fmac_f32_e32 v34, v222, v100
	v_fmac_f32_e32 v36, v226, v100
	v_fmac_f32_e32 v34, v223, v101
	v_fmac_f32_e32 v36, v227, v101
	ds_read_b128 v[98:101], v63 offset:3328
	s_waitcnt lgkmcnt(2)
	v_fmac_f32_e32 v35, v220, v58
	v_fmac_f32_e32 v37, v224, v58
	v_fmac_f32_e32 v35, v221, v59
	v_fmac_f32_e32 v37, v225, v59
	v_fmac_f32_e32 v35, v222, v60
	v_fmac_f32_e32 v37, v226, v60
	v_fmac_f32_e32 v35, v223, v61
	v_fmac_f32_e32 v37, v227, v61
	ds_read_b128 v[58:61], v63 offset:3584
	s_waitcnt lgkmcnt(2)
	v_fmac_f32_e32 v30, v220, v94
	v_fmac_f32_e32 v32, v224, v94
	v_fmac_f32_e32 v30, v221, v95
	v_fmac_f32_e32 v32, v225, v95
	v_fmac_f32_e32 v30, v222, v96
	v_fmac_f32_e32 v32, v226, v96
	v_fmac_f32_e32 v30, v223, v97
	v_fmac_f32_e32 v32, v227, v97
	ds_read_b128 v[94:97], v63 offset:3840
	s_waitcnt lgkmcnt(2)
	v_fmac_f32_e32 v31, v220, v98
	v_fmac_f32_e32 v33, v224, v98
	v_fmac_f32_e32 v31, v221, v99
	v_fmac_f32_e32 v33, v225, v99
	v_fmac_f32_e32 v31, v222, v100
	v_fmac_f32_e32 v33, v226, v100
	v_fmac_f32_e32 v31, v223, v101
	v_fmac_f32_e32 v33, v227, v101
	s_waitcnt lgkmcnt(1)
	v_fmac_f32_e32 v26, v220, v58
	v_fmac_f32_e32 v28, v224, v58
	v_fmac_f32_e32 v26, v221, v59
	v_fmac_f32_e32 v28, v225, v59
	v_fmac_f32_e32 v26, v222, v60
	v_fmac_f32_e32 v28, v226, v60
	v_fmac_f32_e32 v26, v223, v61
	v_fmac_f32_e32 v28, v227, v61
	s_waitcnt lgkmcnt(0)
	v_fmac_f32_e32 v27, v220, v94
	v_fmac_f32_e32 v29, v224, v94
	v_fmac_f32_e32 v27, v221, v95
	v_fmac_f32_e32 v29, v225, v95
	v_fmac_f32_e32 v27, v222, v96
	v_fmac_f32_e32 v29, v226, v96
	v_fmac_f32_e32 v27, v223, v97
	v_fmac_f32_e32 v29, v227, v97
	global_load_dword v220, v62, s[98:99]
	global_load_dword v224, v62, s[98:99] offset:2048
	s_add_u32 s98, s98, 0x1000
	s_addc_u32 s99, s99, 0
	global_load_dword v221, v62, s[98:99]
	global_load_dword v225, v62, s[98:99] offset:2048
	s_add_u32 s98, s98, 0x1000
	s_addc_u32 s99, s99, 0
	global_load_dword v222, v62, s[98:99]
	global_load_dword v226, v62, s[98:99] offset:2048
	s_add_u32 s98, s98, 0x1000
	s_addc_u32 s99, s99, 0
	global_load_dword v223, v62, s[98:99]
	global_load_dword v227, v62, s[98:99] offset:2048
	s_add_u32 s98, s98, 0x1000
	s_addc_u32 s99, s99, 0
	v_mov_b32_e32 v63, s101
	s_add_i32 s101, s101, 16
	ds_read_b128 v[94:97], v63
	ds_read_b128 v[98:101], v63 offset:256
	s_waitcnt vmcnt(24)
	ds_read_b128 v[58:61], v63 offset:512
	s_waitcnt lgkmcnt(2)
	v_fmac_f32_e32 v54, v228, v94
	v_fmac_f32_e32 v56, v232, v94
	v_fmac_f32_e32 v54, v229, v95
	v_fmac_f32_e32 v56, v233, v95
	v_fmac_f32_e32 v54, v230, v96
	v_fmac_f32_e32 v56, v234, v96
	v_fmac_f32_e32 v54, v231, v97
	v_fmac_f32_e32 v56, v235, v97
	ds_read_b128 v[94:97], v63 offset:768
	s_waitcnt lgkmcnt(2)
	v_fmac_f32_e32 v55, v228, v98
	v_fmac_f32_e32 v57, v232, v98
	v_fmac_f32_e32 v55, v229, v99
	v_fmac_f32_e32 v57, v233, v99
	v_fmac_f32_e32 v55, v230, v100
	v_fmac_f32_e32 v57, v234, v100
	v_fmac_f32_e32 v55, v231, v101
	v_fmac_f32_e32 v57, v235, v101
	ds_read_b128 v[98:101], v63 offset:1024
	s_waitcnt lgkmcnt(2)
	v_fmac_f32_e32 v50, v228, v58
	v_fmac_f32_e32 v52, v232, v58
	v_fmac_f32_e32 v50, v229, v59
	v_fmac_f32_e32 v52, v233, v59
	v_fmac_f32_e32 v50, v230, v60
	v_fmac_f32_e32 v52, v234, v60
	v_fmac_f32_e32 v50, v231, v61
	v_fmac_f32_e32 v52, v235, v61
	ds_read_b128 v[58:61], v63 offset:1280
	s_waitcnt lgkmcnt(2)
	v_fmac_f32_e32 v51, v228, v94
	v_fmac_f32_e32 v53, v232, v94
	v_fmac_f32_e32 v51, v229, v95
	v_fmac_f32_e32 v53, v233, v95
	v_fmac_f32_e32 v51, v230, v96
	v_fmac_f32_e32 v53, v234, v96
	v_fmac_f32_e32 v51, v231, v97
	v_fmac_f32_e32 v53, v235, v97
	ds_read_b128 v[94:97], v63 offset:1536
	s_waitcnt lgkmcnt(2)
	v_fmac_f32_e32 v46, v228, v98
	v_fmac_f32_e32 v48, v232, v98
	v_fmac_f32_e32 v46, v229, v99
	v_fmac_f32_e32 v48, v233, v99
	v_fmac_f32_e32 v46, v230, v100
	v_fmac_f32_e32 v48, v234, v100
	v_fmac_f32_e32 v46, v231, v101
	v_fmac_f32_e32 v48, v235, v101
	ds_read_b128 v[98:101], v63 offset:1792
	s_waitcnt lgkmcnt(2)
	v_fmac_f32_e32 v47, v228, v58
	v_fmac_f32_e32 v49, v232, v58
	v_fmac_f32_e32 v47, v229, v59
	v_fmac_f32_e32 v49, v233, v59
	v_fmac_f32_e32 v47, v230, v60
	v_fmac_f32_e32 v49, v234, v60
	v_fmac_f32_e32 v47, v231, v61
	v_fmac_f32_e32 v49, v235, v61
	ds_read_b128 v[58:61], v63 offset:2048
	s_waitcnt lgkmcnt(2)
	v_fmac_f32_e32 v42, v228, v94
	v_fmac_f32_e32 v44, v232, v94
	v_fmac_f32_e32 v42, v229, v95
	v_fmac_f32_e32 v44, v233, v95
	v_fmac_f32_e32 v42, v230, v96
	v_fmac_f32_e32 v44, v234, v96
	v_fmac_f32_e32 v42, v231, v97
	v_fmac_f32_e32 v44, v235, v97
	ds_read_b128 v[94:97], v63 offset:2304
	s_waitcnt lgkmcnt(2)
	v_fmac_f32_e32 v43, v228, v98
	v_fmac_f32_e32 v45, v232, v98
	v_fmac_f32_e32 v43, v229, v99
	v_fmac_f32_e32 v45, v233, v99
	v_fmac_f32_e32 v43, v230, v100
	v_fmac_f32_e32 v45, v234, v100
	v_fmac_f32_e32 v43, v231, v101
	v_fmac_f32_e32 v45, v235, v101
	ds_read_b128 v[98:101], v63 offset:2560
	s_waitcnt lgkmcnt(2)
	v_fmac_f32_e32 v38, v228, v58
	v_fmac_f32_e32 v40, v232, v58
	v_fmac_f32_e32 v38, v229, v59
	v_fmac_f32_e32 v40, v233, v59
	v_fmac_f32_e32 v38, v230, v60
	v_fmac_f32_e32 v40, v234, v60
	v_fmac_f32_e32 v38, v231, v61
	v_fmac_f32_e32 v40, v235, v61
	ds_read_b128 v[58:61], v63 offset:2816
	s_waitcnt lgkmcnt(2)
	v_fmac_f32_e32 v39, v228, v94
	v_fmac_f32_e32 v41, v232, v94
	v_fmac_f32_e32 v39, v229, v95
	v_fmac_f32_e32 v41, v233, v95
	v_fmac_f32_e32 v39, v230, v96
	v_fmac_f32_e32 v41, v234, v96
	v_fmac_f32_e32 v39, v231, v97
	v_fmac_f32_e32 v41, v235, v97
	ds_read_b128 v[94:97], v63 offset:3072
	s_waitcnt lgkmcnt(2)
;     ...
;         for (int k4 = 0; k4 < 16; ++k4) {
;             float wf[4], wb[4];
; #pragma unroll
;             for (int j = 0; j < 4; ++j) { wf[j] = w3[(k4 * 4 + j) * 1024 + tid]; wb[j] = w3[(k4 * 4 + j) * 1024 + 512 + tid]; }
; #pragma unroll
;             for (int pp = 0; pp < 16; ++pp) {
;                 const float4 hv = *(const float4*)&h2[(hp * 16 + pp) * 64 + k4 * 4];
;                 accf[pp] += hv.x * wf[0]; accf[pp] += hv.y * wf[1]; accf[pp] += hv.z * wf[2]; accf[pp] += hv.w * wf[3];
;                 accb[pp] += hv.x * wb[0]; accb[pp] += hv.y * wb[1]; accb[pp] += hv.z * wb[2]; accb[pp] += hv.w * wb[3];
;             }
;         }
	v_fmac_f32_e32 v34, v228, v98
	v_fmac_f32_e32 v36, v232, v98
	v_fmac_f32_e32 v34, v229, v99
	v_fmac_f32_e32 v36, v233, v99
	v_fmac_f32_e32 v34, v230, v100
	v_fmac_f32_e32 v36, v234, v100
	v_fmac_f32_e32 v34, v231, v101
	v_fmac_f32_e32 v36, v235, v101
	ds_read_b128 v[98:101], v63 offset:3328
	s_waitcnt lgkmcnt(2)
	v_fmac_f32_e32 v35, v228, v58
	v_fmac_f32_e32 v37, v232, v58
	v_fmac_f32_e32 v35, v229, v59
	v_fmac_f32_e32 v37, v233, v59
	v_fmac_f32_e32 v35, v230, v60
	v_fmac_f32_e32 v37, v234, v60
	v_fmac_f32_e32 v35, v231, v61
	v_fmac_f32_e32 v37, v235, v61
	ds_read_b128 v[58:61], v63 offset:3584
	s_waitcnt lgkmcnt(2)
	v_fmac_f32_e32 v30, v228, v94
	v_fmac_f32_e32 v32, v232, v94
	v_fmac_f32_e32 v30, v229, v95
	v_fmac_f32_e32 v32, v233, v95
	v_fmac_f32_e32 v30, v230, v96
	v_fmac_f32_e32 v32, v234, v96
	v_fmac_f32_e32 v30, v231, v97
	v_fmac_f32_e32 v32, v235, v97
	ds_read_b128 v[94:97], v63 offset:3840
	s_waitcnt lgkmcnt(2)
	v_fmac_f32_e32 v31, v228, v98
	v_fmac_f32_e32 v33, v232, v98
	v_fmac_f32_e32 v31, v229, v99
	v_fmac_f32_e32 v33, v233, v99
	v_fmac_f32_e32 v31, v230, v100
	v_fmac_f32_e32 v33, v234, v100
	v_fmac_f32_e32 v31, v231, v101
	v_fmac_f32_e32 v33, v235, v101
	s_waitcnt lgkmcnt(1)
	v_fmac_f32_e32 v26, v228, v58
	v_fmac_f32_e32 v28, v232, v58
	v_fmac_f32_e32 v26, v229, v59
	v_fmac_f32_e32 v28, v233, v59
	v_fmac_f32_e32 v26, v230, v60
	v_fmac_f32_e32 v28, v234, v60
	v_fmac_f32_e32 v26, v231, v61
	v_fmac_f32_e32 v28, v235, v61
	s_waitcnt lgkmcnt(0)
	v_fmac_f32_e32 v27, v228, v94
	v_fmac_f32_e32 v29, v232, v94
	v_fmac_f32_e32 v27, v229, v95
	v_fmac_f32_e32 v29, v233, v95
	v_fmac_f32_e32 v27, v230, v96
	v_fmac_f32_e32 v29, v234, v96
	v_fmac_f32_e32 v27, v231, v97
	v_fmac_f32_e32 v29, v235, v97
	global_load_dword v228, v62, s[98:99]
	global_load_dword v232, v62, s[98:99] offset:2048
	s_add_u32 s98, s98, 0x1000
	s_addc_u32 s99, s99, 0
	global_load_dword v229, v62, s[98:99]
	global_load_dword v233, v62, s[98:99] offset:2048
	s_add_u32 s98, s98, 0x1000
	s_addc_u32 s99, s99, 0
	global_load_dword v230, v62, s[98:99]
	global_load_dword v234, v62, s[98:99] offset:2048
	s_add_u32 s98, s98, 0x1000
	s_addc_u32 s99, s99, 0
	global_load_dword v231, v62, s[98:99]
	global_load_dword v235, v62, s[98:99] offset:2048
	s_add_u32 s98, s98, 0x1000
	s_addc_u32 s99, s99, 0
	v_mov_b32_e32 v63, s101
	s_add_i32 s101, s101, 16
	ds_read_b128 v[94:97], v63
	ds_read_b128 v[98:101], v63 offset:256
	s_waitcnt vmcnt(24)
	ds_read_b128 v[58:61], v63 offset:512
	s_waitcnt lgkmcnt(2)
	v_fmac_f32_e32 v54, v204, v94
	v_fmac_f32_e32 v56, v208, v94
	v_fmac_f32_e32 v54, v205, v95
	v_fmac_f32_e32 v56, v209, v95
	v_fmac_f32_e32 v54, v206, v96
	v_fmac_f32_e32 v56, v210, v96
	v_fmac_f32_e32 v54, v207, v97
	v_fmac_f32_e32 v56, v211, v97
	ds_read_b128 v[94:97], v63 offset:768
	s_waitcnt lgkmcnt(2)
	v_fmac_f32_e32 v55, v204, v98
	v_fmac_f32_e32 v57, v208, v98
	v_fmac_f32_e32 v55, v205, v99
	v_fmac_f32_e32 v57, v209, v99
	v_fmac_f32_e32 v55, v206, v100
	v_fmac_f32_e32 v57, v210, v100
	v_fmac_f32_e32 v55, v207, v101
	v_fmac_f32_e32 v57, v211, v101
	ds_read_b128 v[98:101], v63 offset:1024
	s_waitcnt lgkmcnt(2)
	v_fmac_f32_e32 v50, v204, v58
	v_fmac_f32_e32 v52, v208, v58
	v_fmac_f32_e32 v50, v205, v59
	v_fmac_f32_e32 v52, v209, v59
	v_fmac_f32_e32 v50, v206, v60
	v_fmac_f32_e32 v52, v210, v60
	v_fmac_f32_e32 v50, v207, v61
	v_fmac_f32_e32 v52, v211, v61
	ds_read_b128 v[58:61], v63 offset:1280
	s_waitcnt lgkmcnt(2)
	v_fmac_f32_e32 v51, v204, v94
	v_fmac_f32_e32 v53, v208, v94
	v_fmac_f32_e32 v51, v205, v95
	v_fmac_f32_e32 v53, v209, v95
	v_fmac_f32_e32 v51, v206, v96
	v_fmac_f32_e32 v53, v210, v96
	v_fmac_f32_e32 v51, v207, v97
	v_fmac_f32_e32 v53, v211, v97
	ds_read_b128 v[94:97], v63 offset:1536
	s_waitcnt lgkmcnt(2)
	v_fmac_f32_e32 v46, v204, v98
	v_fmac_f32_e32 v48, v208, v98
	v_fmac_f32_e32 v46, v205, v99
	v_fmac_f32_e32 v48, v209, v99
	v_fmac_f32_e32 v46, v206, v100
	v_fmac_f32_e32 v48, v210, v100
	v_fmac_f32_e32 v46, v207, v101
	v_fmac_f32_e32 v48, v211, v101
	ds_read_b128 v[98:101], v63 offset:1792
	s_waitcnt lgkmcnt(2)
	v_fmac_f32_e32 v47, v204, v58
	v_fmac_f32_e32 v49, v208, v58
	v_fmac_f32_e32 v47, v205, v59
	v_fmac_f32_e32 v49, v209, v59
	v_fmac_f32_e32 v47, v206, v60
	v_fmac_f32_e32 v49, v210, v60
	v_fmac_f32_e32 v47, v207, v61
	v_fmac_f32_e32 v49, v211, v61
	ds_read_b128 v[58:61], v63 offset:2048
	s_waitcnt lgkmcnt(2)
	v_fmac_f32_e32 v42, v204, v94
	v_fmac_f32_e32 v44, v208, v94
	v_fmac_f32_e32 v42, v205, v95
	v_fmac_f32_e32 v44, v209, v95
	v_fmac_f32_e32 v42, v206, v96
	v_fmac_f32_e32 v44, v210, v96
	v_fmac_f32_e32 v42, v207, v97
	v_fmac_f32_e32 v44, v211, v97
	ds_read_b128 v[94:97], v63 offset:2304
	s_waitcnt lgkmcnt(2)
	v_fmac_f32_e32 v43, v204, v98
	v_fmac_f32_e32 v45, v208, v98
	v_fmac_f32_e32 v43, v205, v99
	v_fmac_f32_e32 v45, v209, v99
	v_fmac_f32_e32 v43, v206, v100
	v_fmac_f32_e32 v45, v210, v100
	v_fmac_f32_e32 v43, v207, v101
	v_fmac_f32_e32 v45, v211, v101
	ds_read_b128 v[98:101], v63 offset:2560
	s_waitcnt lgkmcnt(2)
	v_fmac_f32_e32 v38, v204, v58
	v_fmac_f32_e32 v40, v208, v58
	v_fmac_f32_e32 v38, v205, v59
	v_fmac_f32_e32 v40, v209, v59
	v_fmac_f32_e32 v38, v206, v60
	v_fmac_f32_e32 v40, v210, v60
	v_fmac_f32_e32 v38, v207, v61
	v_fmac_f32_e32 v40, v211, v61
	ds_read_b128 v[58:61], v63 offset:2816
	s_waitcnt lgkmcnt(2)
	v_fmac_f32_e32 v39, v204, v94
	v_fmac_f32_e32 v41, v208, v94
	v_fmac_f32_e32 v39, v205, v95
	v_fmac_f32_e32 v41, v209, v95
	v_fmac_f32_e32 v39, v206, v96
	v_fmac_f32_e32 v41, v210, v96
	v_fmac_f32_e32 v39, v207, v97
	v_fmac_f32_e32 v41, v211, v97
	ds_read_b128 v[94:97], v63 offset:3072
	s_waitcnt lgkmcnt(2)
;     ...
;         for (int k4 = 0; k4 < 16; ++k4) {
;             float wf[4], wb[4];
; #pragma unroll
;             for (int j = 0; j < 4; ++j) { wf[j] = w3[(k4 * 4 + j) * 1024 + tid]; wb[j] = w3[(k4 * 4 + j) * 1024 + 512 + tid]; }
; #pragma unroll
;             for (int pp = 0; pp < 16; ++pp) {
;                 const float4 hv = *(const float4*)&h2[(hp * 16 + pp) * 64 + k4 * 4];
;                 accf[pp] += hv.x * wf[0]; accf[pp] += hv.y * wf[1]; accf[pp] += hv.z * wf[2]; accf[pp] += hv.w * wf[3];
;                 accb[pp] += hv.x * wb[0]; accb[pp] += hv.y * wb[1]; accb[pp] += hv.z * wb[2]; accb[pp] += hv.w * wb[3];
;             }
;         }
	v_fmac_f32_e32 v34, v204, v98
	v_fmac_f32_e32 v36, v208, v98
	v_fmac_f32_e32 v34, v205, v99
	v_fmac_f32_e32 v36, v209, v99
	v_fmac_f32_e32 v34, v206, v100
	v_fmac_f32_e32 v36, v210, v100
	v_fmac_f32_e32 v34, v207, v101
	v_fmac_f32_e32 v36, v211, v101
	ds_read_b128 v[98:101], v63 offset:3328
	s_waitcnt lgkmcnt(2)
	v_fmac_f32_e32 v35, v204, v58
	v_fmac_f32_e32 v37, v208, v58
	v_fmac_f32_e32 v35, v205, v59
	v_fmac_f32_e32 v37, v209, v59
	v_fmac_f32_e32 v35, v206, v60
	v_fmac_f32_e32 v37, v210, v60
	v_fmac_f32_e32 v35, v207, v61
	v_fmac_f32_e32 v37, v211, v61
	ds_read_b128 v[58:61], v63 offset:3584
	s_waitcnt lgkmcnt(2)
	v_fmac_f32_e32 v30, v204, v94
	v_fmac_f32_e32 v32, v208, v94
	v_fmac_f32_e32 v30, v205, v95
	v_fmac_f32_e32 v32, v209, v95
	v_fmac_f32_e32 v30, v206, v96
	v_fmac_f32_e32 v32, v210, v96
	v_fmac_f32_e32 v30, v207, v97
	v_fmac_f32_e32 v32, v211, v97
	ds_read_b128 v[94:97], v63 offset:3840
	s_waitcnt lgkmcnt(2)
	v_fmac_f32_e32 v31, v204, v98
	v_fmac_f32_e32 v33, v208, v98
	v_fmac_f32_e32 v31, v205, v99
	v_fmac_f32_e32 v33, v209, v99
	v_fmac_f32_e32 v31, v206, v100
	v_fmac_f32_e32 v33, v210, v100
	v_fmac_f32_e32 v31, v207, v101
	v_fmac_f32_e32 v33, v211, v101
	s_waitcnt lgkmcnt(1)
	v_fmac_f32_e32 v26, v204, v58
	v_fmac_f32_e32 v28, v208, v58
	v_fmac_f32_e32 v26, v205, v59
	v_fmac_f32_e32 v28, v209, v59
	v_fmac_f32_e32 v26, v206, v60
	v_fmac_f32_e32 v28, v210, v60
	v_fmac_f32_e32 v26, v207, v61
	v_fmac_f32_e32 v28, v211, v61
	s_waitcnt lgkmcnt(0)
	v_fmac_f32_e32 v27, v204, v94
	v_fmac_f32_e32 v29, v208, v94
	v_fmac_f32_e32 v27, v205, v95
	v_fmac_f32_e32 v29, v209, v95
	v_fmac_f32_e32 v27, v206, v96
	v_fmac_f32_e32 v29, v210, v96
	v_fmac_f32_e32 v27, v207, v97
	v_fmac_f32_e32 v29, v211, v97
	global_load_dword v204, v62, s[98:99]
	global_load_dword v208, v62, s[98:99] offset:2048
	s_add_u32 s98, s98, 0x1000
	s_addc_u32 s99, s99, 0
	global_load_dword v205, v62, s[98:99]
	global_load_dword v209, v62, s[98:99] offset:2048
	s_add_u32 s98, s98, 0x1000
	s_addc_u32 s99, s99, 0
	global_load_dword v206, v62, s[98:99]
	global_load_dword v210, v62, s[98:99] offset:2048
	s_add_u32 s98, s98, 0x1000
	s_addc_u32 s99, s99, 0
	global_load_dword v207, v62, s[98:99]
	global_load_dword v211, v62, s[98:99] offset:2048
	s_add_u32 s98, s98, 0x1000
	s_addc_u32 s99, s99, 0
	v_mov_b32_e32 v63, s101
	s_add_i32 s101, s101, 16
	ds_read_b128 v[94:97], v63
	ds_read_b128 v[98:101], v63 offset:256
	s_waitcnt vmcnt(24)
	ds_read_b128 v[58:61], v63 offset:512
	s_waitcnt lgkmcnt(2)
	v_fmac_f32_e32 v54, v212, v94
	v_fmac_f32_e32 v56, v216, v94
	v_fmac_f32_e32 v54, v213, v95
	v_fmac_f32_e32 v56, v217, v95
	v_fmac_f32_e32 v54, v214, v96
	v_fmac_f32_e32 v56, v218, v96
	v_fmac_f32_e32 v54, v215, v97
	v_fmac_f32_e32 v56, v219, v97
	ds_read_b128 v[94:97], v63 offset:768
	s_waitcnt lgkmcnt(2)
	v_fmac_f32_e32 v55, v212, v98
	v_fmac_f32_e32 v57, v216, v98
	v_fmac_f32_e32 v55, v213, v99
	v_fmac_f32_e32 v57, v217, v99
	v_fmac_f32_e32 v55, v214, v100
	v_fmac_f32_e32 v57, v218, v100
	v_fmac_f32_e32 v55, v215, v101
	v_fmac_f32_e32 v57, v219, v101
	ds_read_b128 v[98:101], v63 offset:1024
	s_waitcnt lgkmcnt(2)
	v_fmac_f32_e32 v50, v212, v58
	v_fmac_f32_e32 v52, v216, v58
	v_fmac_f32_e32 v50, v213, v59
	v_fmac_f32_e32 v52, v217, v59
	v_fmac_f32_e32 v50, v214, v60
	v_fmac_f32_e32 v52, v218, v60
	v_fmac_f32_e32 v50, v215, v61
	v_fmac_f32_e32 v52, v219, v61
	ds_read_b128 v[58:61], v63 offset:1280
	s_waitcnt lgkmcnt(2)
	v_fmac_f32_e32 v51, v212, v94
	v_fmac_f32_e32 v53, v216, v94
	v_fmac_f32_e32 v51, v213, v95
	v_fmac_f32_e32 v53, v217, v95
	v_fmac_f32_e32 v51, v214, v96
	v_fmac_f32_e32 v53, v218, v96
	v_fmac_f32_e32 v51, v215, v97
	v_fmac_f32_e32 v53, v219, v97
	ds_read_b128 v[94:97], v63 offset:1536
	s_waitcnt lgkmcnt(2)
	v_fmac_f32_e32 v46, v212, v98
	v_fmac_f32_e32 v48, v216, v98
	v_fmac_f32_e32 v46, v213, v99
	v_fmac_f32_e32 v48, v217, v99
	v_fmac_f32_e32 v46, v214, v100
	v_fmac_f32_e32 v48, v218, v100
	v_fmac_f32_e32 v46, v215, v101
	v_fmac_f32_e32 v48, v219, v101
	ds_read_b128 v[98:101], v63 offset:1792
	s_waitcnt lgkmcnt(2)
	v_fmac_f32_e32 v47, v212, v58
	v_fmac_f32_e32 v49, v216, v58
	v_fmac_f32_e32 v47, v213, v59
	v_fmac_f32_e32 v49, v217, v59
	v_fmac_f32_e32 v47, v214, v60
	v_fmac_f32_e32 v49, v218, v60
	v_fmac_f32_e32 v47, v215, v61
	v_fmac_f32_e32 v49, v219, v61
	ds_read_b128 v[58:61], v63 offset:2048
	s_waitcnt lgkmcnt(2)
	v_fmac_f32_e32 v42, v212, v94
	v_fmac_f32_e32 v44, v216, v94
	v_fmac_f32_e32 v42, v213, v95
	v_fmac_f32_e32 v44, v217, v95
	v_fmac_f32_e32 v42, v214, v96
	v_fmac_f32_e32 v44, v218, v96
	v_fmac_f32_e32 v42, v215, v97
	v_fmac_f32_e32 v44, v219, v97
	ds_read_b128 v[94:97], v63 offset:2304
	s_waitcnt lgkmcnt(2)
	v_fmac_f32_e32 v43, v212, v98
	v_fmac_f32_e32 v45, v216, v98
	v_fmac_f32_e32 v43, v213, v99
	v_fmac_f32_e32 v45, v217, v99
	v_fmac_f32_e32 v43, v214, v100
	v_fmac_f32_e32 v45, v218, v100
	v_fmac_f32_e32 v43, v215, v101
	v_fmac_f32_e32 v45, v219, v101
	ds_read_b128 v[98:101], v63 offset:2560
	s_waitcnt lgkmcnt(2)
	v_fmac_f32_e32 v38, v212, v58
	v_fmac_f32_e32 v40, v216, v58
	v_fmac_f32_e32 v38, v213, v59
	v_fmac_f32_e32 v40, v217, v59
	v_fmac_f32_e32 v38, v214, v60
	v_fmac_f32_e32 v40, v218, v60
	v_fmac_f32_e32 v38, v215, v61
	v_fmac_f32_e32 v40, v219, v61
	ds_read_b128 v[58:61], v63 offset:2816
	s_waitcnt lgkmcnt(2)
	v_fmac_f32_e32 v39, v212, v94
	v_fmac_f32_e32 v41, v216, v94
	v_fmac_f32_e32 v39, v213, v95
	v_fmac_f32_e32 v41, v217, v95
	v_fmac_f32_e32 v39, v214, v96
	v_fmac_f32_e32 v41, v218, v96
	v_fmac_f32_e32 v39, v215, v97
	v_fmac_f32_e32 v41, v219, v97
	ds_read_b128 v[94:97], v63 offset:3072
	s_waitcnt lgkmcnt(2)
;     ...
;         for (int k4 = 0; k4 < 16; ++k4) {
;             float wf[4], wb[4];
; #pragma unroll
;             for (int j = 0; j < 4; ++j) { wf[j] = w3[(k4 * 4 + j) * 1024 + tid]; wb[j] = w3[(k4 * 4 + j) * 1024 + 512 + tid]; }
; #pragma unroll
;             for (int pp = 0; pp < 16; ++pp) {
;                 const float4 hv = *(const float4*)&h2[(hp * 16 + pp) * 64 + k4 * 4];
;                 accf[pp] += hv.x * wf[0]; accf[pp] += hv.y * wf[1]; accf[pp] += hv.z * wf[2]; accf[pp] += hv.w * wf[3];
;                 accb[pp] += hv.x * wb[0]; accb[pp] += hv.y * wb[1]; accb[pp] += hv.z * wb[2]; accb[pp] += hv.w * wb[3];
;             }
;         }
	v_fmac_f32_e32 v34, v212, v98
	v_fmac_f32_e32 v36, v216, v98
	v_fmac_f32_e32 v34, v213, v99
	v_fmac_f32_e32 v36, v217, v99
	v_fmac_f32_e32 v34, v214, v100
	v_fmac_f32_e32 v36, v218, v100
	v_fmac_f32_e32 v34, v215, v101
	v_fmac_f32_e32 v36, v219, v101
	ds_read_b128 v[98:101], v63 offset:3328
	s_waitcnt lgkmcnt(2)
	v_fmac_f32_e32 v35, v212, v58
	v_fmac_f32_e32 v37, v216, v58
	v_fmac_f32_e32 v35, v213, v59
	v_fmac_f32_e32 v37, v217, v59
	v_fmac_f32_e32 v35, v214, v60
	v_fmac_f32_e32 v37, v218, v60
	v_fmac_f32_e32 v35, v215, v61
	v_fmac_f32_e32 v37, v219, v61
	ds_read_b128 v[58:61], v63 offset:3584
	s_waitcnt lgkmcnt(2)
	v_fmac_f32_e32 v30, v212, v94
	v_fmac_f32_e32 v32, v216, v94
	v_fmac_f32_e32 v30, v213, v95
	v_fmac_f32_e32 v32, v217, v95
	v_fmac_f32_e32 v30, v214, v96
	v_fmac_f32_e32 v32, v218, v96
	v_fmac_f32_e32 v30, v215, v97
	v_fmac_f32_e32 v32, v219, v97
	ds_read_b128 v[94:97], v63 offset:3840
	s_waitcnt lgkmcnt(2)
	v_fmac_f32_e32 v31, v212, v98
	v_fmac_f32_e32 v33, v216, v98
	v_fmac_f32_e32 v31, v213, v99
	v_fmac_f32_e32 v33, v217, v99
	v_fmac_f32_e32 v31, v214, v100
	v_fmac_f32_e32 v33, v218, v100
	v_fmac_f32_e32 v31, v215, v101
	v_fmac_f32_e32 v33, v219, v101
	s_waitcnt lgkmcnt(1)
	v_fmac_f32_e32 v26, v212, v58
	v_fmac_f32_e32 v28, v216, v58
	v_fmac_f32_e32 v26, v213, v59
	v_fmac_f32_e32 v28, v217, v59
	v_fmac_f32_e32 v26, v214, v60
	v_fmac_f32_e32 v28, v218, v60
	v_fmac_f32_e32 v26, v215, v61
	v_fmac_f32_e32 v28, v219, v61
	s_waitcnt lgkmcnt(0)
	v_fmac_f32_e32 v27, v212, v94
	v_fmac_f32_e32 v29, v216, v94
	v_fmac_f32_e32 v27, v213, v95
	v_fmac_f32_e32 v29, v217, v95
	v_fmac_f32_e32 v27, v214, v96
	v_fmac_f32_e32 v29, v218, v96
	v_fmac_f32_e32 v27, v215, v97
	v_fmac_f32_e32 v29, v219, v97
	global_load_dword v212, v62, s[98:99]
	global_load_dword v216, v62, s[98:99] offset:2048
	s_add_u32 s98, s98, 0x1000
	s_addc_u32 s99, s99, 0
	global_load_dword v213, v62, s[98:99]
	global_load_dword v217, v62, s[98:99] offset:2048
	s_add_u32 s98, s98, 0x1000
	s_addc_u32 s99, s99, 0
	global_load_dword v214, v62, s[98:99]
	global_load_dword v218, v62, s[98:99] offset:2048
	s_add_u32 s98, s98, 0x1000
	s_addc_u32 s99, s99, 0
	global_load_dword v215, v62, s[98:99]
	global_load_dword v219, v62, s[98:99] offset:2048
	s_add_u32 s98, s98, 0x1000
	s_addc_u32 s99, s99, 0
	v_mov_b32_e32 v63, s101
	s_add_i32 s101, s101, 16
	ds_read_b128 v[94:97], v63
	ds_read_b128 v[98:101], v63 offset:256
	s_waitcnt vmcnt(24)
	ds_read_b128 v[58:61], v63 offset:512
	s_waitcnt lgkmcnt(2)
	v_fmac_f32_e32 v54, v220, v94
	v_fmac_f32_e32 v56, v224, v94
	v_fmac_f32_e32 v54, v221, v95
	v_fmac_f32_e32 v56, v225, v95
	v_fmac_f32_e32 v54, v222, v96
	v_fmac_f32_e32 v56, v226, v96
	v_fmac_f32_e32 v54, v223, v97
	v_fmac_f32_e32 v56, v227, v97
	ds_read_b128 v[94:97], v63 offset:768
	s_waitcnt lgkmcnt(2)
	v_fmac_f32_e32 v55, v220, v98
	v_fmac_f32_e32 v57, v224, v98
	v_fmac_f32_e32 v55, v221, v99
	v_fmac_f32_e32 v57, v225, v99
	v_fmac_f32_e32 v55, v222, v100
	v_fmac_f32_e32 v57, v226, v100
	v_fmac_f32_e32 v55, v223, v101
	v_fmac_f32_e32 v57, v227, v101
	ds_read_b128 v[98:101], v63 offset:1024
	s_waitcnt lgkmcnt(2)
	v_fmac_f32_e32 v50, v220, v58
	v_fmac_f32_e32 v52, v224, v58
	v_fmac_f32_e32 v50, v221, v59
	v_fmac_f32_e32 v52, v225, v59
	v_fmac_f32_e32 v50, v222, v60
	v_fmac_f32_e32 v52, v226, v60
	v_fmac_f32_e32 v50, v223, v61
	v_fmac_f32_e32 v52, v227, v61
	ds_read_b128 v[58:61], v63 offset:1280
	s_waitcnt lgkmcnt(2)
	v_fmac_f32_e32 v51, v220, v94
	v_fmac_f32_e32 v53, v224, v94
	v_fmac_f32_e32 v51, v221, v95
	v_fmac_f32_e32 v53, v225, v95
	v_fmac_f32_e32 v51, v222, v96
	v_fmac_f32_e32 v53, v226, v96
	v_fmac_f32_e32 v51, v223, v97
	v_fmac_f32_e32 v53, v227, v97
	ds_read_b128 v[94:97], v63 offset:1536
	s_waitcnt lgkmcnt(2)
	v_fmac_f32_e32 v46, v220, v98
	v_fmac_f32_e32 v48, v224, v98
	v_fmac_f32_e32 v46, v221, v99
	v_fmac_f32_e32 v48, v225, v99
	v_fmac_f32_e32 v46, v222, v100
	v_fmac_f32_e32 v48, v226, v100
	v_fmac_f32_e32 v46, v223, v101
	v_fmac_f32_e32 v48, v227, v101
	ds_read_b128 v[98:101], v63 offset:1792
	s_waitcnt lgkmcnt(2)
	v_fmac_f32_e32 v47, v220, v58
	v_fmac_f32_e32 v49, v224, v58
	v_fmac_f32_e32 v47, v221, v59
	v_fmac_f32_e32 v49, v225, v59
	v_fmac_f32_e32 v47, v222, v60
	v_fmac_f32_e32 v49, v226, v60
	v_fmac_f32_e32 v47, v223, v61
	v_fmac_f32_e32 v49, v227, v61
	ds_read_b128 v[58:61], v63 offset:2048
	s_waitcnt lgkmcnt(2)
	v_fmac_f32_e32 v42, v220, v94
	v_fmac_f32_e32 v44, v224, v94
	v_fmac_f32_e32 v42, v221, v95
	v_fmac_f32_e32 v44, v225, v95
	v_fmac_f32_e32 v42, v222, v96
	v_fmac_f32_e32 v44, v226, v96
	v_fmac_f32_e32 v42, v223, v97
	v_fmac_f32_e32 v44, v227, v97
	ds_read_b128 v[94:97], v63 offset:2304
	s_waitcnt lgkmcnt(2)
	v_fmac_f32_e32 v43, v220, v98
	v_fmac_f32_e32 v45, v224, v98
	v_fmac_f32_e32 v43, v221, v99
	v_fmac_f32_e32 v45, v225, v99
	v_fmac_f32_e32 v43, v222, v100
	v_fmac_f32_e32 v45, v226, v100
	v_fmac_f32_e32 v43, v223, v101
	v_fmac_f32_e32 v45, v227, v101
	ds_read_b128 v[98:101], v63 offset:2560
	s_waitcnt lgkmcnt(2)
	v_fmac_f32_e32 v38, v220, v58
	v_fmac_f32_e32 v40, v224, v58
	v_fmac_f32_e32 v38, v221, v59
	v_fmac_f32_e32 v40, v225, v59
	v_fmac_f32_e32 v38, v222, v60
	v_fmac_f32_e32 v40, v226, v60
	v_fmac_f32_e32 v38, v223, v61
	v_fmac_f32_e32 v40, v227, v61
	ds_read_b128 v[58:61], v63 offset:2816
	s_waitcnt lgkmcnt(2)
	v_fmac_f32_e32 v39, v220, v94
	v_fmac_f32_e32 v41, v224, v94
	v_fmac_f32_e32 v39, v221, v95
	v_fmac_f32_e32 v41, v225, v95
	v_fmac_f32_e32 v39, v222, v96
	v_fmac_f32_e32 v41, v226, v96
	v_fmac_f32_e32 v39, v223, v97
	v_fmac_f32_e32 v41, v227, v97
	ds_read_b128 v[94:97], v63 offset:3072
	s_waitcnt lgkmcnt(2)
;     ...
;         for (int k4 = 0; k4 < 16; ++k4) {
;             float wf[4], wb[4];
; #pragma unroll
;             for (int j = 0; j < 4; ++j) { wf[j] = w3[(k4 * 4 + j) * 1024 + tid]; wb[j] = w3[(k4 * 4 + j) * 1024 + 512 + tid]; }
; #pragma unroll
;             for (int pp = 0; pp < 16; ++pp) {
;                 const float4 hv = *(const float4*)&h2[(hp * 16 + pp) * 64 + k4 * 4];
;                 accf[pp] += hv.x * wf[0]; accf[pp] += hv.y * wf[1]; accf[pp] += hv.z * wf[2]; accf[pp] += hv.w * wf[3];
;                 accb[pp] += hv.x * wb[0]; accb[pp] += hv.y * wb[1]; accb[pp] += hv.z * wb[2]; accb[pp] += hv.w * wb[3];
;             }
;         }
	v_fmac_f32_e32 v34, v220, v98
	v_fmac_f32_e32 v36, v224, v98
	v_fmac_f32_e32 v34, v221, v99
	v_fmac_f32_e32 v36, v225, v99
	v_fmac_f32_e32 v34, v222, v100
	v_fmac_f32_e32 v36, v226, v100
	v_fmac_f32_e32 v34, v223, v101
	v_fmac_f32_e32 v36, v227, v101
	ds_read_b128 v[98:101], v63 offset:3328
	s_waitcnt lgkmcnt(2)
	v_fmac_f32_e32 v35, v220, v58
	v_fmac_f32_e32 v37, v224, v58
	v_fmac_f32_e32 v35, v221, v59
	v_fmac_f32_e32 v37, v225, v59
	v_fmac_f32_e32 v35, v222, v60
	v_fmac_f32_e32 v37, v226, v60
	v_fmac_f32_e32 v35, v223, v61
	v_fmac_f32_e32 v37, v227, v61
	ds_read_b128 v[58:61], v63 offset:3584
	s_waitcnt lgkmcnt(2)
	v_fmac_f32_e32 v30, v220, v94
	v_fmac_f32_e32 v32, v224, v94
	v_fmac_f32_e32 v30, v221, v95
	v_fmac_f32_e32 v32, v225, v95
	v_fmac_f32_e32 v30, v222, v96
	v_fmac_f32_e32 v32, v226, v96
	v_fmac_f32_e32 v30, v223, v97
	v_fmac_f32_e32 v32, v227, v97
	ds_read_b128 v[94:97], v63 offset:3840
	s_waitcnt lgkmcnt(2)
	v_fmac_f32_e32 v31, v220, v98
	v_fmac_f32_e32 v33, v224, v98
	v_fmac_f32_e32 v31, v221, v99
	v_fmac_f32_e32 v33, v225, v99
	v_fmac_f32_e32 v31, v222, v100
	v_fmac_f32_e32 v33, v226, v100
	v_fmac_f32_e32 v31, v223, v101
	v_fmac_f32_e32 v33, v227, v101
	s_waitcnt lgkmcnt(1)
	v_fmac_f32_e32 v26, v220, v58
	v_fmac_f32_e32 v28, v224, v58
	v_fmac_f32_e32 v26, v221, v59
	v_fmac_f32_e32 v28, v225, v59
	v_fmac_f32_e32 v26, v222, v60
	v_fmac_f32_e32 v28, v226, v60
	v_fmac_f32_e32 v26, v223, v61
	v_fmac_f32_e32 v28, v227, v61
	s_waitcnt lgkmcnt(0)
	v_fmac_f32_e32 v27, v220, v94
	v_fmac_f32_e32 v29, v224, v94
	v_fmac_f32_e32 v27, v221, v95
	v_fmac_f32_e32 v29, v225, v95
	v_fmac_f32_e32 v27, v222, v96
	v_fmac_f32_e32 v29, v226, v96
	v_fmac_f32_e32 v27, v223, v97
	v_fmac_f32_e32 v29, v227, v97
	global_load_dword v220, v62, s[98:99]
	global_load_dword v224, v62, s[98:99] offset:2048
	s_add_u32 s98, s98, 0x1000
	s_addc_u32 s99, s99, 0
	global_load_dword v221, v62, s[98:99]
	global_load_dword v225, v62, s[98:99] offset:2048
	s_add_u32 s98, s98, 0x1000
	s_addc_u32 s99, s99, 0
	global_load_dword v222, v62, s[98:99]
	global_load_dword v226, v62, s[98:99] offset:2048
	s_add_u32 s98, s98, 0x1000
	s_addc_u32 s99, s99, 0
	global_load_dword v223, v62, s[98:99]
	global_load_dword v227, v62, s[98:99] offset:2048
	s_add_u32 s98, s98, 0x1000
	s_addc_u32 s99, s99, 0
	v_mov_b32_e32 v63, s101
	s_add_i32 s101, s101, 16
	ds_read_b128 v[94:97], v63
	ds_read_b128 v[98:101], v63 offset:256
	s_waitcnt vmcnt(24)
	ds_read_b128 v[58:61], v63 offset:512
	s_waitcnt lgkmcnt(2)
	v_fmac_f32_e32 v54, v228, v94
	v_fmac_f32_e32 v56, v232, v94
	v_fmac_f32_e32 v54, v229, v95
	v_fmac_f32_e32 v56, v233, v95
	v_fmac_f32_e32 v54, v230, v96
	v_fmac_f32_e32 v56, v234, v96
	v_fmac_f32_e32 v54, v231, v97
	v_fmac_f32_e32 v56, v235, v97
	ds_read_b128 v[94:97], v63 offset:768
	s_waitcnt lgkmcnt(2)
	v_fmac_f32_e32 v55, v228, v98
	v_fmac_f32_e32 v57, v232, v98
	v_fmac_f32_e32 v55, v229, v99
	v_fmac_f32_e32 v57, v233, v99
	v_fmac_f32_e32 v55, v230, v100
	v_fmac_f32_e32 v57, v234, v100
	v_fmac_f32_e32 v55, v231, v101
	v_fmac_f32_e32 v57, v235, v101
	ds_read_b128 v[98:101], v63 offset:1024
	s_waitcnt lgkmcnt(2)
	v_fmac_f32_e32 v50, v228, v58
	v_fmac_f32_e32 v52, v232, v58
	v_fmac_f32_e32 v50, v229, v59
	v_fmac_f32_e32 v52, v233, v59
	v_fmac_f32_e32 v50, v230, v60
	v_fmac_f32_e32 v52, v234, v60
	v_fmac_f32_e32 v50, v231, v61
	v_fmac_f32_e32 v52, v235, v61
	ds_read_b128 v[58:61], v63 offset:1280
	s_waitcnt lgkmcnt(2)
	v_fmac_f32_e32 v51, v228, v94
	v_fmac_f32_e32 v53, v232, v94
	v_fmac_f32_e32 v51, v229, v95
	v_fmac_f32_e32 v53, v233, v95
	v_fmac_f32_e32 v51, v230, v96
	v_fmac_f32_e32 v53, v234, v96
	v_fmac_f32_e32 v51, v231, v97
	v_fmac_f32_e32 v53, v235, v97
	ds_read_b128 v[94:97], v63 offset:1536
	s_waitcnt lgkmcnt(2)
	v_fmac_f32_e32 v46, v228, v98
	v_fmac_f32_e32 v48, v232, v98
	v_fmac_f32_e32 v46, v229, v99
	v_fmac_f32_e32 v48, v233, v99
	v_fmac_f32_e32 v46, v230, v100
	v_fmac_f32_e32 v48, v234, v100
	v_fmac_f32_e32 v46, v231, v101
	v_fmac_f32_e32 v48, v235, v101
	ds_read_b128 v[98:101], v63 offset:1792
	s_waitcnt lgkmcnt(2)
	v_fmac_f32_e32 v47, v228, v58
	v_fmac_f32_e32 v49, v232, v58
	v_fmac_f32_e32 v47, v229, v59
	v_fmac_f32_e32 v49, v233, v59
	v_fmac_f32_e32 v47, v230, v60
	v_fmac_f32_e32 v49, v234, v60
	v_fmac_f32_e32 v47, v231, v61
	v_fmac_f32_e32 v49, v235, v61
	ds_read_b128 v[58:61], v63 offset:2048
	s_waitcnt lgkmcnt(2)
	v_fmac_f32_e32 v42, v228, v94
	v_fmac_f32_e32 v44, v232, v94
	v_fmac_f32_e32 v42, v229, v95
	v_fmac_f32_e32 v44, v233, v95
	v_fmac_f32_e32 v42, v230, v96
	v_fmac_f32_e32 v44, v234, v96
	v_fmac_f32_e32 v42, v231, v97
	v_fmac_f32_e32 v44, v235, v97
	ds_read_b128 v[94:97], v63 offset:2304
	s_waitcnt lgkmcnt(2)
	v_fmac_f32_e32 v43, v228, v98
	v_fmac_f32_e32 v45, v232, v98
	v_fmac_f32_e32 v43, v229, v99
	v_fmac_f32_e32 v45, v233, v99
	v_fmac_f32_e32 v43, v230, v100
	v_fmac_f32_e32 v45, v234, v100
	v_fmac_f32_e32 v43, v231, v101
	v_fmac_f32_e32 v45, v235, v101
	ds_read_b128 v[98:101], v63 offset:2560
	s_waitcnt lgkmcnt(2)
	v_fmac_f32_e32 v38, v228, v58
	v_fmac_f32_e32 v40, v232, v58
	v_fmac_f32_e32 v38, v229, v59
	v_fmac_f32_e32 v40, v233, v59
	v_fmac_f32_e32 v38, v230, v60
	v_fmac_f32_e32 v40, v234, v60
	v_fmac_f32_e32 v38, v231, v61
	v_fmac_f32_e32 v40, v235, v61
	ds_read_b128 v[58:61], v63 offset:2816
	s_waitcnt lgkmcnt(2)
	v_fmac_f32_e32 v39, v228, v94
	v_fmac_f32_e32 v41, v232, v94
	v_fmac_f32_e32 v39, v229, v95
	v_fmac_f32_e32 v41, v233, v95
	v_fmac_f32_e32 v39, v230, v96
	v_fmac_f32_e32 v41, v234, v96
	v_fmac_f32_e32 v39, v231, v97
	v_fmac_f32_e32 v41, v235, v97
	ds_read_b128 v[94:97], v63 offset:3072
	s_waitcnt lgkmcnt(2)
;     ...
;         for (int k4 = 0; k4 < 16; ++k4) {
;             float wf[4], wb[4];
; #pragma unroll
;             for (int j = 0; j < 4; ++j) { wf[j] = w3[(k4 * 4 + j) * 1024 + tid]; wb[j] = w3[(k4 * 4 + j) * 1024 + 512 + tid]; }
; #pragma unroll
;             for (int pp = 0; pp < 16; ++pp) {
;                 const float4 hv = *(const float4*)&h2[(hp * 16 + pp) * 64 + k4 * 4];
;                 accf[pp] += hv.x * wf[0]; accf[pp] += hv.y * wf[1]; accf[pp] += hv.z * wf[2]; accf[pp] += hv.w * wf[3];
;                 accb[pp] += hv.x * wb[0]; accb[pp] += hv.y * wb[1]; accb[pp] += hv.z * wb[2]; accb[pp] += hv.w * wb[3];
;             }
;         }
	v_fmac_f32_e32 v34, v228, v98
	v_fmac_f32_e32 v36, v232, v98
	v_fmac_f32_e32 v34, v229, v99
	v_fmac_f32_e32 v36, v233, v99
	v_fmac_f32_e32 v34, v230, v100
	v_fmac_f32_e32 v36, v234, v100
	v_fmac_f32_e32 v34, v231, v101
	v_fmac_f32_e32 v36, v235, v101
	ds_read_b128 v[98:101], v63 offset:3328
	s_waitcnt lgkmcnt(2)
	v_fmac_f32_e32 v35, v228, v58
	v_fmac_f32_e32 v37, v232, v58
	v_fmac_f32_e32 v35, v229, v59
	v_fmac_f32_e32 v37, v233, v59
	v_fmac_f32_e32 v35, v230, v60
	v_fmac_f32_e32 v37, v234, v60
	v_fmac_f32_e32 v35, v231, v61
	v_fmac_f32_e32 v37, v235, v61
	ds_read_b128 v[58:61], v63 offset:3584
	s_waitcnt lgkmcnt(2)
	v_fmac_f32_e32 v30, v228, v94
	v_fmac_f32_e32 v32, v232, v94
	v_fmac_f32_e32 v30, v229, v95
	v_fmac_f32_e32 v32, v233, v95
	v_fmac_f32_e32 v30, v230, v96
	v_fmac_f32_e32 v32, v234, v96
	v_fmac_f32_e32 v30, v231, v97
	v_fmac_f32_e32 v32, v235, v97
	ds_read_b128 v[94:97], v63 offset:3840
	s_waitcnt lgkmcnt(2)
	v_fmac_f32_e32 v31, v228, v98
	v_fmac_f32_e32 v33, v232, v98
	v_fmac_f32_e32 v31, v229, v99
	v_fmac_f32_e32 v33, v233, v99
	v_fmac_f32_e32 v31, v230, v100
	v_fmac_f32_e32 v33, v234, v100
	v_fmac_f32_e32 v31, v231, v101
	v_fmac_f32_e32 v33, v235, v101
	s_waitcnt lgkmcnt(1)
	v_fmac_f32_e32 v26, v228, v58
	v_fmac_f32_e32 v28, v232, v58
	v_fmac_f32_e32 v26, v229, v59
	v_fmac_f32_e32 v28, v233, v59
	v_fmac_f32_e32 v26, v230, v60
	v_fmac_f32_e32 v28, v234, v60
	v_fmac_f32_e32 v26, v231, v61
	v_fmac_f32_e32 v28, v235, v61
	s_waitcnt lgkmcnt(0)
	v_fmac_f32_e32 v27, v228, v94
	v_fmac_f32_e32 v29, v232, v94
	v_fmac_f32_e32 v27, v229, v95
	v_fmac_f32_e32 v29, v233, v95
	v_fmac_f32_e32 v27, v230, v96
	v_fmac_f32_e32 v29, v234, v96
	v_fmac_f32_e32 v27, v231, v97
	v_fmac_f32_e32 v29, v235, v97
	global_load_dword v228, v62, s[98:99]
	global_load_dword v232, v62, s[98:99] offset:2048
	s_add_u32 s98, s98, 0x1000
	s_addc_u32 s99, s99, 0
	global_load_dword v229, v62, s[98:99]
	global_load_dword v233, v62, s[98:99] offset:2048
	s_add_u32 s98, s98, 0x1000
	s_addc_u32 s99, s99, 0
	global_load_dword v230, v62, s[98:99]
	global_load_dword v234, v62, s[98:99] offset:2048
	s_add_u32 s98, s98, 0x1000
	s_addc_u32 s99, s99, 0
	global_load_dword v231, v62, s[98:99]
	global_load_dword v235, v62, s[98:99] offset:2048
	s_add_u32 s98, s98, 0x1000
	s_addc_u32 s99, s99, 0
	v_mov_b32_e32 v63, s101
	s_add_i32 s101, s101, 16
	ds_read_b128 v[94:97], v63
	ds_read_b128 v[98:101], v63 offset:256
	s_waitcnt vmcnt(24)
	ds_read_b128 v[58:61], v63 offset:512
	s_waitcnt lgkmcnt(2)
	v_fmac_f32_e32 v54, v204, v94
	v_fmac_f32_e32 v56, v208, v94
	v_fmac_f32_e32 v54, v205, v95
	v_fmac_f32_e32 v56, v209, v95
	v_fmac_f32_e32 v54, v206, v96
	v_fmac_f32_e32 v56, v210, v96
	v_fmac_f32_e32 v54, v207, v97
	v_fmac_f32_e32 v56, v211, v97
	ds_read_b128 v[94:97], v63 offset:768
	s_waitcnt lgkmcnt(2)
	v_fmac_f32_e32 v55, v204, v98
	v_fmac_f32_e32 v57, v208, v98
	v_fmac_f32_e32 v55, v205, v99
	v_fmac_f32_e32 v57, v209, v99
	v_fmac_f32_e32 v55, v206, v100
	v_fmac_f32_e32 v57, v210, v100
	v_fmac_f32_e32 v55, v207, v101
	v_fmac_f32_e32 v57, v211, v101
	ds_read_b128 v[98:101], v63 offset:1024
	s_waitcnt lgkmcnt(2)
	v_fmac_f32_e32 v50, v204, v58
	v_fmac_f32_e32 v52, v208, v58
	v_fmac_f32_e32 v50, v205, v59
	v_fmac_f32_e32 v52, v209, v59
	v_fmac_f32_e32 v50, v206, v60
	v_fmac_f32_e32 v52, v210, v60
	v_fmac_f32_e32 v50, v207, v61
	v_fmac_f32_e32 v52, v211, v61
	ds_read_b128 v[58:61], v63 offset:1280
	s_waitcnt lgkmcnt(2)
	v_fmac_f32_e32 v51, v204, v94
	v_fmac_f32_e32 v53, v208, v94
	v_fmac_f32_e32 v51, v205, v95
	v_fmac_f32_e32 v53, v209, v95
	v_fmac_f32_e32 v51, v206, v96
	v_fmac_f32_e32 v53, v210, v96
	v_fmac_f32_e32 v51, v207, v97
	v_fmac_f32_e32 v53, v211, v97
	ds_read_b128 v[94:97], v63 offset:1536
	s_waitcnt lgkmcnt(2)
	v_fmac_f32_e32 v46, v204, v98
	v_fmac_f32_e32 v48, v208, v98
	v_fmac_f32_e32 v46, v205, v99
	v_fmac_f32_e32 v48, v209, v99
	v_fmac_f32_e32 v46, v206, v100
	v_fmac_f32_e32 v48, v210, v100
	v_fmac_f32_e32 v46, v207, v101
	v_fmac_f32_e32 v48, v211, v101
	ds_read_b128 v[98:101], v63 offset:1792
	s_waitcnt lgkmcnt(2)
	v_fmac_f32_e32 v47, v204, v58
	v_fmac_f32_e32 v49, v208, v58
	v_fmac_f32_e32 v47, v205, v59
	v_fmac_f32_e32 v49, v209, v59
	v_fmac_f32_e32 v47, v206, v60
	v_fmac_f32_e32 v49, v210, v60
	v_fmac_f32_e32 v47, v207, v61
	v_fmac_f32_e32 v49, v211, v61
	ds_read_b128 v[58:61], v63 offset:2048
	s_waitcnt lgkmcnt(2)
	v_fmac_f32_e32 v42, v204, v94
	v_fmac_f32_e32 v44, v208, v94
	v_fmac_f32_e32 v42, v205, v95
	v_fmac_f32_e32 v44, v209, v95
	v_fmac_f32_e32 v42, v206, v96
	v_fmac_f32_e32 v44, v210, v96
	v_fmac_f32_e32 v42, v207, v97
	v_fmac_f32_e32 v44, v211, v97
	ds_read_b128 v[94:97], v63 offset:2304
	s_waitcnt lgkmcnt(2)
	v_fmac_f32_e32 v43, v204, v98
	v_fmac_f32_e32 v45, v208, v98
	v_fmac_f32_e32 v43, v205, v99
	v_fmac_f32_e32 v45, v209, v99
	v_fmac_f32_e32 v43, v206, v100
	v_fmac_f32_e32 v45, v210, v100
	v_fmac_f32_e32 v43, v207, v101
	v_fmac_f32_e32 v45, v211, v101
	ds_read_b128 v[98:101], v63 offset:2560
	s_waitcnt lgkmcnt(2)
	v_fmac_f32_e32 v38, v204, v58
	v_fmac_f32_e32 v40, v208, v58
	v_fmac_f32_e32 v38, v205, v59
	v_fmac_f32_e32 v40, v209, v59
	v_fmac_f32_e32 v38, v206, v60
	v_fmac_f32_e32 v40, v210, v60
	v_fmac_f32_e32 v38, v207, v61
	v_fmac_f32_e32 v40, v211, v61
	ds_read_b128 v[58:61], v63 offset:2816
	s_waitcnt lgkmcnt(2)
	v_fmac_f32_e32 v39, v204, v94
	v_fmac_f32_e32 v41, v208, v94
	v_fmac_f32_e32 v39, v205, v95
	v_fmac_f32_e32 v41, v209, v95
	v_fmac_f32_e32 v39, v206, v96
	v_fmac_f32_e32 v41, v210, v96
	v_fmac_f32_e32 v39, v207, v97
	v_fmac_f32_e32 v41, v211, v97
	ds_read_b128 v[94:97], v63 offset:3072
	s_waitcnt lgkmcnt(2)
;     ...
;         for (int k4 = 0; k4 < 16; ++k4) {
;             float wf[4], wb[4];
; #pragma unroll
;             for (int j = 0; j < 4; ++j) { wf[j] = w3[(k4 * 4 + j) * 1024 + tid]; wb[j] = w3[(k4 * 4 + j) * 1024 + 512 + tid]; }
; #pragma unroll
;             for (int pp = 0; pp < 16; ++pp) {
;                 const float4 hv = *(const float4*)&h2[(hp * 16 + pp) * 64 + k4 * 4];
;                 accf[pp] += hv.x * wf[0]; accf[pp] += hv.y * wf[1]; accf[pp] += hv.z * wf[2]; accf[pp] += hv.w * wf[3];
;                 accb[pp] += hv.x * wb[0]; accb[pp] += hv.y * wb[1]; accb[pp] += hv.z * wb[2]; accb[pp] += hv.w * wb[3];
;             }
;         }
	v_fmac_f32_e32 v34, v204, v98
	v_fmac_f32_e32 v36, v208, v98
	v_fmac_f32_e32 v34, v205, v99
	v_fmac_f32_e32 v36, v209, v99
	v_fmac_f32_e32 v34, v206, v100
	v_fmac_f32_e32 v36, v210, v100
	v_fmac_f32_e32 v34, v207, v101
	v_fmac_f32_e32 v36, v211, v101
	ds_read_b128 v[98:101], v63 offset:3328
	s_waitcnt lgkmcnt(2)
	v_fmac_f32_e32 v35, v204, v58
	v_fmac_f32_e32 v37, v208, v58
	v_fmac_f32_e32 v35, v205, v59
	v_fmac_f32_e32 v37, v209, v59
	v_fmac_f32_e32 v35, v206, v60
	v_fmac_f32_e32 v37, v210, v60
	v_fmac_f32_e32 v35, v207, v61
	v_fmac_f32_e32 v37, v211, v61
	ds_read_b128 v[58:61], v63 offset:3584
	s_waitcnt lgkmcnt(2)
	v_fmac_f32_e32 v30, v204, v94
	v_fmac_f32_e32 v32, v208, v94
	v_fmac_f32_e32 v30, v205, v95
	v_fmac_f32_e32 v32, v209, v95
	v_fmac_f32_e32 v30, v206, v96
	v_fmac_f32_e32 v32, v210, v96
	v_fmac_f32_e32 v30, v207, v97
	v_fmac_f32_e32 v32, v211, v97
	ds_read_b128 v[94:97], v63 offset:3840
	s_waitcnt lgkmcnt(2)
	v_fmac_f32_e32 v31, v204, v98
	v_fmac_f32_e32 v33, v208, v98
	v_fmac_f32_e32 v31, v205, v99
	v_fmac_f32_e32 v33, v209, v99
	v_fmac_f32_e32 v31, v206, v100
	v_fmac_f32_e32 v33, v210, v100
	v_fmac_f32_e32 v31, v207, v101
	v_fmac_f32_e32 v33, v211, v101
	s_waitcnt lgkmcnt(1)
	v_fmac_f32_e32 v26, v204, v58
	v_fmac_f32_e32 v28, v208, v58
	v_fmac_f32_e32 v26, v205, v59
	v_fmac_f32_e32 v28, v209, v59
	v_fmac_f32_e32 v26, v206, v60
	v_fmac_f32_e32 v28, v210, v60
	v_fmac_f32_e32 v26, v207, v61
	v_fmac_f32_e32 v28, v211, v61
	s_waitcnt lgkmcnt(0)
	v_fmac_f32_e32 v27, v204, v94
	v_fmac_f32_e32 v29, v208, v94
	v_fmac_f32_e32 v27, v205, v95
	v_fmac_f32_e32 v29, v209, v95
	v_fmac_f32_e32 v27, v206, v96
	v_fmac_f32_e32 v29, v210, v96
	v_fmac_f32_e32 v27, v207, v97
	v_fmac_f32_e32 v29, v211, v97
	global_load_dword v204, v62, s[98:99]
	global_load_dword v208, v62, s[98:99] offset:2048
	s_add_u32 s98, s98, 0x1000
	s_addc_u32 s99, s99, 0
	global_load_dword v205, v62, s[98:99]
	global_load_dword v209, v62, s[98:99] offset:2048
	s_add_u32 s98, s98, 0x1000
	s_addc_u32 s99, s99, 0
	global_load_dword v206, v62, s[98:99]
	global_load_dword v210, v62, s[98:99] offset:2048
	s_add_u32 s98, s98, 0x1000
	s_addc_u32 s99, s99, 0
	global_load_dword v207, v62, s[98:99]
	global_load_dword v211, v62, s[98:99] offset:2048
	s_add_u32 s98, s98, 0x1000
	s_addc_u32 s99, s99, 0
	v_mov_b32_e32 v63, s101
	s_add_i32 s101, s101, 16
	ds_read_b128 v[94:97], v63
	ds_read_b128 v[98:101], v63 offset:256
	s_waitcnt vmcnt(24)
	ds_read_b128 v[58:61], v63 offset:512
	s_waitcnt lgkmcnt(2)
	v_fmac_f32_e32 v54, v212, v94
	v_fmac_f32_e32 v56, v216, v94
	v_fmac_f32_e32 v54, v213, v95
	v_fmac_f32_e32 v56, v217, v95
	v_fmac_f32_e32 v54, v214, v96
	v_fmac_f32_e32 v56, v218, v96
	v_fmac_f32_e32 v54, v215, v97
	v_fmac_f32_e32 v56, v219, v97
	ds_read_b128 v[94:97], v63 offset:768
	s_waitcnt lgkmcnt(2)
	v_fmac_f32_e32 v55, v212, v98
	v_fmac_f32_e32 v57, v216, v98
	v_fmac_f32_e32 v55, v213, v99
	v_fmac_f32_e32 v57, v217, v99
	v_fmac_f32_e32 v55, v214, v100
	v_fmac_f32_e32 v57, v218, v100
	v_fmac_f32_e32 v55, v215, v101
	v_fmac_f32_e32 v57, v219, v101
	ds_read_b128 v[98:101], v63 offset:1024
	s_waitcnt lgkmcnt(2)
	v_fmac_f32_e32 v50, v212, v58
	v_fmac_f32_e32 v52, v216, v58
	v_fmac_f32_e32 v50, v213, v59
	v_fmac_f32_e32 v52, v217, v59
	v_fmac_f32_e32 v50, v214, v60
	v_fmac_f32_e32 v52, v218, v60
	v_fmac_f32_e32 v50, v215, v61
	v_fmac_f32_e32 v52, v219, v61
	ds_read_b128 v[58:61], v63 offset:1280
	s_waitcnt lgkmcnt(2)
	v_fmac_f32_e32 v51, v212, v94
	v_fmac_f32_e32 v53, v216, v94
	v_fmac_f32_e32 v51, v213, v95
	v_fmac_f32_e32 v53, v217, v95
	v_fmac_f32_e32 v51, v214, v96
	v_fmac_f32_e32 v53, v218, v96
	v_fmac_f32_e32 v51, v215, v97
	v_fmac_f32_e32 v53, v219, v97
	ds_read_b128 v[94:97], v63 offset:1536
	s_waitcnt lgkmcnt(2)
	v_fmac_f32_e32 v46, v212, v98
	v_fmac_f32_e32 v48, v216, v98
	v_fmac_f32_e32 v46, v213, v99
	v_fmac_f32_e32 v48, v217, v99
	v_fmac_f32_e32 v46, v214, v100
	v_fmac_f32_e32 v48, v218, v100
	v_fmac_f32_e32 v46, v215, v101
	v_fmac_f32_e32 v48, v219, v101
	ds_read_b128 v[98:101], v63 offset:1792
	s_waitcnt lgkmcnt(2)
	v_fmac_f32_e32 v47, v212, v58
	v_fmac_f32_e32 v49, v216, v58
	v_fmac_f32_e32 v47, v213, v59
	v_fmac_f32_e32 v49, v217, v59
	v_fmac_f32_e32 v47, v214, v60
	v_fmac_f32_e32 v49, v218, v60
	v_fmac_f32_e32 v47, v215, v61
	v_fmac_f32_e32 v49, v219, v61
	ds_read_b128 v[58:61], v63 offset:2048
	s_waitcnt lgkmcnt(2)
	v_fmac_f32_e32 v42, v212, v94
	v_fmac_f32_e32 v44, v216, v94
	v_fmac_f32_e32 v42, v213, v95
	v_fmac_f32_e32 v44, v217, v95
	v_fmac_f32_e32 v42, v214, v96
	v_fmac_f32_e32 v44, v218, v96
	v_fmac_f32_e32 v42, v215, v97
	v_fmac_f32_e32 v44, v219, v97
	ds_read_b128 v[94:97], v63 offset:2304
	s_waitcnt lgkmcnt(2)
	v_fmac_f32_e32 v43, v212, v98
	v_fmac_f32_e32 v45, v216, v98
	v_fmac_f32_e32 v43, v213, v99
	v_fmac_f32_e32 v45, v217, v99
	v_fmac_f32_e32 v43, v214, v100
	v_fmac_f32_e32 v45, v218, v100
	v_fmac_f32_e32 v43, v215, v101
	v_fmac_f32_e32 v45, v219, v101
	ds_read_b128 v[98:101], v63 offset:2560
	s_waitcnt lgkmcnt(2)
	v_fmac_f32_e32 v38, v212, v58
	v_fmac_f32_e32 v40, v216, v58
	v_fmac_f32_e32 v38, v213, v59
	v_fmac_f32_e32 v40, v217, v59
	v_fmac_f32_e32 v38, v214, v60
	v_fmac_f32_e32 v40, v218, v60
	v_fmac_f32_e32 v38, v215, v61
	v_fmac_f32_e32 v40, v219, v61
	ds_read_b128 v[58:61], v63 offset:2816
	s_waitcnt lgkmcnt(2)
	v_fmac_f32_e32 v39, v212, v94
	v_fmac_f32_e32 v41, v216, v94
	v_fmac_f32_e32 v39, v213, v95
	v_fmac_f32_e32 v41, v217, v95
	v_fmac_f32_e32 v39, v214, v96
	v_fmac_f32_e32 v41, v218, v96
	v_fmac_f32_e32 v39, v215, v97
	v_fmac_f32_e32 v41, v219, v97
	ds_read_b128 v[94:97], v63 offset:3072
	s_waitcnt lgkmcnt(2)
;     ...
;         for (int k4 = 0; k4 < 16; ++k4) {
;             float wf[4], wb[4];
; #pragma unroll
;             for (int j = 0; j < 4; ++j) { wf[j] = w3[(k4 * 4 + j) * 1024 + tid]; wb[j] = w3[(k4 * 4 + j) * 1024 + 512 + tid]; }
; #pragma unroll
;             for (int pp = 0; pp < 16; ++pp) {
;                 const float4 hv = *(const float4*)&h2[(hp * 16 + pp) * 64 + k4 * 4];
;                 accf[pp] += hv.x * wf[0]; accf[pp] += hv.y * wf[1]; accf[pp] += hv.z * wf[2]; accf[pp] += hv.w * wf[3];
;                 accb[pp] += hv.x * wb[0]; accb[pp] += hv.y * wb[1]; accb[pp] += hv.z * wb[2]; accb[pp] += hv.w * wb[3];
;             }
;         }
	v_fmac_f32_e32 v34, v212, v98
	v_fmac_f32_e32 v36, v216, v98
	v_fmac_f32_e32 v34, v213, v99
	v_fmac_f32_e32 v36, v217, v99
	v_fmac_f32_e32 v34, v214, v100
	v_fmac_f32_e32 v36, v218, v100
	v_fmac_f32_e32 v34, v215, v101
	v_fmac_f32_e32 v36, v219, v101
	ds_read_b128 v[98:101], v63 offset:3328
	s_waitcnt lgkmcnt(2)
	v_fmac_f32_e32 v35, v212, v58
	v_fmac_f32_e32 v37, v216, v58
	v_fmac_f32_e32 v35, v213, v59
	v_fmac_f32_e32 v37, v217, v59
	v_fmac_f32_e32 v35, v214, v60
	v_fmac_f32_e32 v37, v218, v60
	v_fmac_f32_e32 v35, v215, v61
	v_fmac_f32_e32 v37, v219, v61
	ds_read_b128 v[58:61], v63 offset:3584
	s_waitcnt lgkmcnt(2)
	v_fmac_f32_e32 v30, v212, v94
	v_fmac_f32_e32 v32, v216, v94
	v_fmac_f32_e32 v30, v213, v95
	v_fmac_f32_e32 v32, v217, v95
	v_fmac_f32_e32 v30, v214, v96
	v_fmac_f32_e32 v32, v218, v96
	v_fmac_f32_e32 v30, v215, v97
	v_fmac_f32_e32 v32, v219, v97
	ds_read_b128 v[94:97], v63 offset:3840
	s_waitcnt lgkmcnt(2)
	v_fmac_f32_e32 v31, v212, v98
	v_fmac_f32_e32 v33, v216, v98
	v_fmac_f32_e32 v31, v213, v99
	v_fmac_f32_e32 v33, v217, v99
	v_fmac_f32_e32 v31, v214, v100
	v_fmac_f32_e32 v33, v218, v100
	v_fmac_f32_e32 v31, v215, v101
	v_fmac_f32_e32 v33, v219, v101
	s_waitcnt lgkmcnt(1)
	v_fmac_f32_e32 v26, v212, v58
	v_fmac_f32_e32 v28, v216, v58
	v_fmac_f32_e32 v26, v213, v59
	v_fmac_f32_e32 v28, v217, v59
	v_fmac_f32_e32 v26, v214, v60
	v_fmac_f32_e32 v28, v218, v60
	v_fmac_f32_e32 v26, v215, v61
	v_fmac_f32_e32 v28, v219, v61
	s_waitcnt lgkmcnt(0)
	v_fmac_f32_e32 v27, v212, v94
	v_fmac_f32_e32 v29, v216, v94
	v_fmac_f32_e32 v27, v213, v95
	v_fmac_f32_e32 v29, v217, v95
	v_fmac_f32_e32 v27, v214, v96
	v_fmac_f32_e32 v29, v218, v96
	v_fmac_f32_e32 v27, v215, v97
	v_fmac_f32_e32 v29, v219, v97
	global_load_dword v212, v62, s[98:99]
	global_load_dword v216, v62, s[98:99] offset:2048
	s_add_u32 s98, s98, 0x1000
	s_addc_u32 s99, s99, 0
	global_load_dword v213, v62, s[98:99]
	global_load_dword v217, v62, s[98:99] offset:2048
	s_add_u32 s98, s98, 0x1000
	s_addc_u32 s99, s99, 0
	global_load_dword v214, v62, s[98:99]
	global_load_dword v218, v62, s[98:99] offset:2048
	s_add_u32 s98, s98, 0x1000
	s_addc_u32 s99, s99, 0
	global_load_dword v215, v62, s[98:99]
	global_load_dword v219, v62, s[98:99] offset:2048
	s_add_u32 s98, s98, 0x1000
	s_addc_u32 s99, s99, 0
	v_mov_b32_e32 v63, s101
	s_add_i32 s101, s101, 16
	ds_read_b128 v[94:97], v63
	ds_read_b128 v[98:101], v63 offset:256
	s_waitcnt vmcnt(24)
	ds_read_b128 v[58:61], v63 offset:512
	s_waitcnt lgkmcnt(2)
	v_fmac_f32_e32 v54, v220, v94
	v_fmac_f32_e32 v56, v224, v94
	v_fmac_f32_e32 v54, v221, v95
	v_fmac_f32_e32 v56, v225, v95
	v_fmac_f32_e32 v54, v222, v96
	v_fmac_f32_e32 v56, v226, v96
	v_fmac_f32_e32 v54, v223, v97
	v_fmac_f32_e32 v56, v227, v97
	ds_read_b128 v[94:97], v63 offset:768
	s_waitcnt lgkmcnt(2)
	v_fmac_f32_e32 v55, v220, v98
	v_fmac_f32_e32 v57, v224, v98
	v_fmac_f32_e32 v55, v221, v99
	v_fmac_f32_e32 v57, v225, v99
	v_fmac_f32_e32 v55, v222, v100
	v_fmac_f32_e32 v57, v226, v100
	v_fmac_f32_e32 v55, v223, v101
	v_fmac_f32_e32 v57, v227, v101
	ds_read_b128 v[98:101], v63 offset:1024
	s_waitcnt lgkmcnt(2)
	v_fmac_f32_e32 v50, v220, v58
	v_fmac_f32_e32 v52, v224, v58
	v_fmac_f32_e32 v50, v221, v59
	v_fmac_f32_e32 v52, v225, v59
	v_fmac_f32_e32 v50, v222, v60
	v_fmac_f32_e32 v52, v226, v60
	v_fmac_f32_e32 v50, v223, v61
	v_fmac_f32_e32 v52, v227, v61
	ds_read_b128 v[58:61], v63 offset:1280
	s_waitcnt lgkmcnt(2)
	v_fmac_f32_e32 v51, v220, v94
	v_fmac_f32_e32 v53, v224, v94
	v_fmac_f32_e32 v51, v221, v95
	v_fmac_f32_e32 v53, v225, v95
	v_fmac_f32_e32 v51, v222, v96
	v_fmac_f32_e32 v53, v226, v96
	v_fmac_f32_e32 v51, v223, v97
	v_fmac_f32_e32 v53, v227, v97
	ds_read_b128 v[94:97], v63 offset:1536
	s_waitcnt lgkmcnt(2)
	v_fmac_f32_e32 v46, v220, v98
	v_fmac_f32_e32 v48, v224, v98
	v_fmac_f32_e32 v46, v221, v99
	v_fmac_f32_e32 v48, v225, v99
	v_fmac_f32_e32 v46, v222, v100
	v_fmac_f32_e32 v48, v226, v100
	v_fmac_f32_e32 v46, v223, v101
	v_fmac_f32_e32 v48, v227, v101
	ds_read_b128 v[98:101], v63 offset:1792
	s_waitcnt lgkmcnt(2)
	v_fmac_f32_e32 v47, v220, v58
	v_fmac_f32_e32 v49, v224, v58
	v_fmac_f32_e32 v47, v221, v59
	v_fmac_f32_e32 v49, v225, v59
	v_fmac_f32_e32 v47, v222, v60
	v_fmac_f32_e32 v49, v226, v60
	v_fmac_f32_e32 v47, v223, v61
	v_fmac_f32_e32 v49, v227, v61
	ds_read_b128 v[58:61], v63 offset:2048
	s_waitcnt lgkmcnt(2)
	v_fmac_f32_e32 v42, v220, v94
	v_fmac_f32_e32 v44, v224, v94
	v_fmac_f32_e32 v42, v221, v95
	v_fmac_f32_e32 v44, v225, v95
	v_fmac_f32_e32 v42, v222, v96
	v_fmac_f32_e32 v44, v226, v96
	v_fmac_f32_e32 v42, v223, v97
	v_fmac_f32_e32 v44, v227, v97
	ds_read_b128 v[94:97], v63 offset:2304
	s_waitcnt lgkmcnt(2)
	v_fmac_f32_e32 v43, v220, v98
	v_fmac_f32_e32 v45, v224, v98
	v_fmac_f32_e32 v43, v221, v99
	v_fmac_f32_e32 v45, v225, v99
	v_fmac_f32_e32 v43, v222, v100
	v_fmac_f32_e32 v45, v226, v100
	v_fmac_f32_e32 v43, v223, v101
	v_fmac_f32_e32 v45, v227, v101
	ds_read_b128 v[98:101], v63 offset:2560
	s_waitcnt lgkmcnt(2)
	v_fmac_f32_e32 v38, v220, v58
	v_fmac_f32_e32 v40, v224, v58
	v_fmac_f32_e32 v38, v221, v59
	v_fmac_f32_e32 v40, v225, v59
	v_fmac_f32_e32 v38, v222, v60
	v_fmac_f32_e32 v40, v226, v60
	v_fmac_f32_e32 v38, v223, v61
	v_fmac_f32_e32 v40, v227, v61
	ds_read_b128 v[58:61], v63 offset:2816
	s_waitcnt lgkmcnt(2)
	v_fmac_f32_e32 v39, v220, v94
	v_fmac_f32_e32 v41, v224, v94
	v_fmac_f32_e32 v39, v221, v95
	v_fmac_f32_e32 v41, v225, v95
	v_fmac_f32_e32 v39, v222, v96
	v_fmac_f32_e32 v41, v226, v96
	v_fmac_f32_e32 v39, v223, v97
	v_fmac_f32_e32 v41, v227, v97
	ds_read_b128 v[94:97], v63 offset:3072
	s_waitcnt lgkmcnt(2)
;     ...
;         for (int k4 = 0; k4 < 16; ++k4) {
;             float wf[4], wb[4];
; #pragma unroll
;             for (int j = 0; j < 4; ++j) { wf[j] = w3[(k4 * 4 + j) * 1024 + tid]; wb[j] = w3[(k4 * 4 + j) * 1024 + 512 + tid]; }
; #pragma unroll
;             for (int pp = 0; pp < 16; ++pp) {
;                 const float4 hv = *(const float4*)&h2[(hp * 16 + pp) * 64 + k4 * 4];
;                 accf[pp] += hv.x * wf[0]; accf[pp] += hv.y * wf[1]; accf[pp] += hv.z * wf[2]; accf[pp] += hv.w * wf[3];
;                 accb[pp] += hv.x * wb[0]; accb[pp] += hv.y * wb[1]; accb[pp] += hv.z * wb[2]; accb[pp] += hv.w * wb[3];
;             }
;         }
	v_fmac_f32_e32 v34, v220, v98
	v_fmac_f32_e32 v36, v224, v98
	v_fmac_f32_e32 v34, v221, v99
	v_fmac_f32_e32 v36, v225, v99
	v_fmac_f32_e32 v34, v222, v100
	v_fmac_f32_e32 v36, v226, v100
	v_fmac_f32_e32 v34, v223, v101
	v_fmac_f32_e32 v36, v227, v101
	ds_read_b128 v[98:101], v63 offset:3328
	s_waitcnt lgkmcnt(2)
	v_fmac_f32_e32 v35, v220, v58
	v_fmac_f32_e32 v37, v224, v58
	v_fmac_f32_e32 v35, v221, v59
	v_fmac_f32_e32 v37, v225, v59
	v_fmac_f32_e32 v35, v222, v60
	v_fmac_f32_e32 v37, v226, v60
	v_fmac_f32_e32 v35, v223, v61
	v_fmac_f32_e32 v37, v227, v61
	ds_read_b128 v[58:61], v63 offset:3584
	s_waitcnt lgkmcnt(2)
	v_fmac_f32_e32 v30, v220, v94
	v_fmac_f32_e32 v32, v224, v94
	v_fmac_f32_e32 v30, v221, v95
	v_fmac_f32_e32 v32, v225, v95
	v_fmac_f32_e32 v30, v222, v96
	v_fmac_f32_e32 v32, v226, v96
	v_fmac_f32_e32 v30, v223, v97
	v_fmac_f32_e32 v32, v227, v97
	ds_read_b128 v[94:97], v63 offset:3840
	s_waitcnt lgkmcnt(2)
	v_fmac_f32_e32 v31, v220, v98
	v_fmac_f32_e32 v33, v224, v98
	v_fmac_f32_e32 v31, v221, v99
	v_fmac_f32_e32 v33, v225, v99
	v_fmac_f32_e32 v31, v222, v100
	v_fmac_f32_e32 v33, v226, v100
	v_fmac_f32_e32 v31, v223, v101
	v_fmac_f32_e32 v33, v227, v101
	s_waitcnt lgkmcnt(1)
	v_fmac_f32_e32 v26, v220, v58
	v_fmac_f32_e32 v28, v224, v58
	v_fmac_f32_e32 v26, v221, v59
	v_fmac_f32_e32 v28, v225, v59
	v_fmac_f32_e32 v26, v222, v60
	v_fmac_f32_e32 v28, v226, v60
	v_fmac_f32_e32 v26, v223, v61
	v_fmac_f32_e32 v28, v227, v61
	s_waitcnt lgkmcnt(0)
	v_fmac_f32_e32 v27, v220, v94
	v_fmac_f32_e32 v29, v224, v94
	v_fmac_f32_e32 v27, v221, v95
	v_fmac_f32_e32 v29, v225, v95
	v_fmac_f32_e32 v27, v222, v96
	v_fmac_f32_e32 v29, v226, v96
	v_fmac_f32_e32 v27, v223, v97
	v_fmac_f32_e32 v29, v227, v97
	global_load_dword v220, v62, s[98:99]
	global_load_dword v224, v62, s[98:99] offset:2048
	s_add_u32 s98, s98, 0x1000
	s_addc_u32 s99, s99, 0
	global_load_dword v221, v62, s[98:99]
	global_load_dword v225, v62, s[98:99] offset:2048
	s_add_u32 s98, s98, 0x1000
	s_addc_u32 s99, s99, 0
	global_load_dword v222, v62, s[98:99]
	global_load_dword v226, v62, s[98:99] offset:2048
	s_add_u32 s98, s98, 0x1000
	s_addc_u32 s99, s99, 0
	global_load_dword v223, v62, s[98:99]
	global_load_dword v227, v62, s[98:99] offset:2048
	s_add_u32 s98, s98, 0x1000
	s_addc_u32 s99, s99, 0
	v_mov_b32_e32 v63, s101
	s_add_i32 s101, s101, 16
	ds_read_b128 v[94:97], v63
	ds_read_b128 v[98:101], v63 offset:256
	s_waitcnt vmcnt(24)
	ds_read_b128 v[58:61], v63 offset:512
	s_waitcnt lgkmcnt(2)
	v_fmac_f32_e32 v54, v228, v94
	v_fmac_f32_e32 v56, v232, v94
	v_fmac_f32_e32 v54, v229, v95
	v_fmac_f32_e32 v56, v233, v95
	v_fmac_f32_e32 v54, v230, v96
	v_fmac_f32_e32 v56, v234, v96
	v_fmac_f32_e32 v54, v231, v97
	v_fmac_f32_e32 v56, v235, v97
	ds_read_b128 v[94:97], v63 offset:768
	s_waitcnt lgkmcnt(2)
	v_fmac_f32_e32 v55, v228, v98
	v_fmac_f32_e32 v57, v232, v98
	v_fmac_f32_e32 v55, v229, v99
	v_fmac_f32_e32 v57, v233, v99
	v_fmac_f32_e32 v55, v230, v100
	v_fmac_f32_e32 v57, v234, v100
	v_fmac_f32_e32 v55, v231, v101
	v_fmac_f32_e32 v57, v235, v101
	ds_read_b128 v[98:101], v63 offset:1024
	s_waitcnt lgkmcnt(2)
	v_fmac_f32_e32 v50, v228, v58
	v_fmac_f32_e32 v52, v232, v58
	v_fmac_f32_e32 v50, v229, v59
	v_fmac_f32_e32 v52, v233, v59
	v_fmac_f32_e32 v50, v230, v60
	v_fmac_f32_e32 v52, v234, v60
	v_fmac_f32_e32 v50, v231, v61
	v_fmac_f32_e32 v52, v235, v61
	ds_read_b128 v[58:61], v63 offset:1280
	s_waitcnt lgkmcnt(2)
	v_fmac_f32_e32 v51, v228, v94
	v_fmac_f32_e32 v53, v232, v94
	v_fmac_f32_e32 v51, v229, v95
	v_fmac_f32_e32 v53, v233, v95
	v_fmac_f32_e32 v51, v230, v96
	v_fmac_f32_e32 v53, v234, v96
	v_fmac_f32_e32 v51, v231, v97
	v_fmac_f32_e32 v53, v235, v97
	ds_read_b128 v[94:97], v63 offset:1536
	s_waitcnt lgkmcnt(2)
	v_fmac_f32_e32 v46, v228, v98
	v_fmac_f32_e32 v48, v232, v98
	v_fmac_f32_e32 v46, v229, v99
	v_fmac_f32_e32 v48, v233, v99
	v_fmac_f32_e32 v46, v230, v100
	v_fmac_f32_e32 v48, v234, v100
	v_fmac_f32_e32 v46, v231, v101
	v_fmac_f32_e32 v48, v235, v101
	ds_read_b128 v[98:101], v63 offset:1792
	s_waitcnt lgkmcnt(2)
	v_fmac_f32_e32 v47, v228, v58
	v_fmac_f32_e32 v49, v232, v58
	v_fmac_f32_e32 v47, v229, v59
	v_fmac_f32_e32 v49, v233, v59
	v_fmac_f32_e32 v47, v230, v60
	v_fmac_f32_e32 v49, v234, v60
	v_fmac_f32_e32 v47, v231, v61
	v_fmac_f32_e32 v49, v235, v61
	ds_read_b128 v[58:61], v63 offset:2048
	s_waitcnt lgkmcnt(2)
	v_fmac_f32_e32 v42, v228, v94
	v_fmac_f32_e32 v44, v232, v94
	v_fmac_f32_e32 v42, v229, v95
	v_fmac_f32_e32 v44, v233, v95
	v_fmac_f32_e32 v42, v230, v96
	v_fmac_f32_e32 v44, v234, v96
	v_fmac_f32_e32 v42, v231, v97
	v_fmac_f32_e32 v44, v235, v97
	ds_read_b128 v[94:97], v63 offset:2304
	s_waitcnt lgkmcnt(2)
	v_fmac_f32_e32 v43, v228, v98
	v_fmac_f32_e32 v45, v232, v98
	v_fmac_f32_e32 v43, v229, v99
	v_fmac_f32_e32 v45, v233, v99
	v_fmac_f32_e32 v43, v230, v100
	v_fmac_f32_e32 v45, v234, v100
	v_fmac_f32_e32 v43, v231, v101
	v_fmac_f32_e32 v45, v235, v101
	ds_read_b128 v[98:101], v63 offset:2560
	s_waitcnt lgkmcnt(2)
	v_fmac_f32_e32 v38, v228, v58
	v_fmac_f32_e32 v40, v232, v58
	v_fmac_f32_e32 v38, v229, v59
	v_fmac_f32_e32 v40, v233, v59
	v_fmac_f32_e32 v38, v230, v60
	v_fmac_f32_e32 v40, v234, v60
	v_fmac_f32_e32 v38, v231, v61
	v_fmac_f32_e32 v40, v235, v61
	ds_read_b128 v[58:61], v63 offset:2816
	s_waitcnt lgkmcnt(2)
	v_fmac_f32_e32 v39, v228, v94
	v_fmac_f32_e32 v41, v232, v94
	v_fmac_f32_e32 v39, v229, v95
	v_fmac_f32_e32 v41, v233, v95
	v_fmac_f32_e32 v39, v230, v96
	v_fmac_f32_e32 v41, v234, v96
	v_fmac_f32_e32 v39, v231, v97
	v_fmac_f32_e32 v41, v235, v97
	ds_read_b128 v[94:97], v63 offset:3072
	s_waitcnt lgkmcnt(2)
;     ...
;         for (int k4 = 0; k4 < 16; ++k4) {
;             float wf[4], wb[4];
; #pragma unroll
;             for (int j = 0; j < 4; ++j) { wf[j] = w3[(k4 * 4 + j) * 1024 + tid]; wb[j] = w3[(k4 * 4 + j) * 1024 + 512 + tid]; }
; #pragma unroll
;             for (int pp = 0; pp < 16; ++pp) {
;                 const float4 hv = *(const float4*)&h2[(hp * 16 + pp) * 64 + k4 * 4];
;                 accf[pp] += hv.x * wf[0]; accf[pp] += hv.y * wf[1]; accf[pp] += hv.z * wf[2]; accf[pp] += hv.w * wf[3];
;                 accb[pp] += hv.x * wb[0]; accb[pp] += hv.y * wb[1]; accb[pp] += hv.z * wb[2]; accb[pp] += hv.w * wb[3];
;             }
;         }
	v_fmac_f32_e32 v34, v228, v98
	v_fmac_f32_e32 v36, v232, v98
	v_fmac_f32_e32 v34, v229, v99
	v_fmac_f32_e32 v36, v233, v99
	v_fmac_f32_e32 v34, v230, v100
	v_fmac_f32_e32 v36, v234, v100
	v_fmac_f32_e32 v34, v231, v101
	v_fmac_f32_e32 v36, v235, v101
	ds_read_b128 v[98:101], v63 offset:3328
	s_waitcnt lgkmcnt(2)
	v_fmac_f32_e32 v35, v228, v58
	v_fmac_f32_e32 v37, v232, v58
	v_fmac_f32_e32 v35, v229, v59
	v_fmac_f32_e32 v37, v233, v59
	v_fmac_f32_e32 v35, v230, v60
	v_fmac_f32_e32 v37, v234, v60
	v_fmac_f32_e32 v35, v231, v61
	v_fmac_f32_e32 v37, v235, v61
	ds_read_b128 v[58:61], v63 offset:3584
	s_waitcnt lgkmcnt(2)
	v_fmac_f32_e32 v30, v228, v94
	v_fmac_f32_e32 v32, v232, v94
	v_fmac_f32_e32 v30, v229, v95
	v_fmac_f32_e32 v32, v233, v95
	v_fmac_f32_e32 v30, v230, v96
	v_fmac_f32_e32 v32, v234, v96
	v_fmac_f32_e32 v30, v231, v97
	v_fmac_f32_e32 v32, v235, v97
	ds_read_b128 v[94:97], v63 offset:3840
	s_waitcnt lgkmcnt(2)
	v_fmac_f32_e32 v31, v228, v98
	v_fmac_f32_e32 v33, v232, v98
	v_fmac_f32_e32 v31, v229, v99
	v_fmac_f32_e32 v33, v233, v99
	v_fmac_f32_e32 v31, v230, v100
	v_fmac_f32_e32 v33, v234, v100
	v_fmac_f32_e32 v31, v231, v101
	v_fmac_f32_e32 v33, v235, v101
	s_waitcnt lgkmcnt(1)
	v_fmac_f32_e32 v26, v228, v58
	v_fmac_f32_e32 v28, v232, v58
	v_fmac_f32_e32 v26, v229, v59
	v_fmac_f32_e32 v28, v233, v59
	v_fmac_f32_e32 v26, v230, v60
	v_fmac_f32_e32 v28, v234, v60
	v_fmac_f32_e32 v26, v231, v61
	v_fmac_f32_e32 v28, v235, v61
	s_waitcnt lgkmcnt(0)
	v_fmac_f32_e32 v27, v228, v94
	v_fmac_f32_e32 v29, v232, v94
	v_fmac_f32_e32 v27, v229, v95
	v_fmac_f32_e32 v29, v233, v95
	v_fmac_f32_e32 v27, v230, v96
	v_fmac_f32_e32 v29, v234, v96
	v_fmac_f32_e32 v27, v231, v97
	v_fmac_f32_e32 v29, v235, v97
	global_load_dword v228, v62, s[98:99]
	global_load_dword v232, v62, s[98:99] offset:2048
	s_add_u32 s98, s98, 0x1000
	s_addc_u32 s99, s99, 0
	global_load_dword v229, v62, s[98:99]
	global_load_dword v233, v62, s[98:99] offset:2048
	s_add_u32 s98, s98, 0x1000
	s_addc_u32 s99, s99, 0
	global_load_dword v230, v62, s[98:99]
	global_load_dword v234, v62, s[98:99] offset:2048
	s_add_u32 s98, s98, 0x1000
	s_addc_u32 s99, s99, 0
	global_load_dword v231, v62, s[98:99]
	global_load_dword v235, v62, s[98:99] offset:2048
	s_add_u32 s98, s98, 0x1000
	s_addc_u32 s99, s99, 0
	v_mov_b32_e32 v63, s101
	s_add_i32 s101, s101, 16
	ds_read_b128 v[94:97], v63
	ds_read_b128 v[98:101], v63 offset:256
	s_waitcnt vmcnt(24)
	ds_read_b128 v[58:61], v63 offset:512
	s_waitcnt lgkmcnt(2)
	v_fmac_f32_e32 v54, v204, v94
	v_fmac_f32_e32 v56, v208, v94
	v_fmac_f32_e32 v54, v205, v95
	v_fmac_f32_e32 v56, v209, v95
	v_fmac_f32_e32 v54, v206, v96
	v_fmac_f32_e32 v56, v210, v96
	v_fmac_f32_e32 v54, v207, v97
	v_fmac_f32_e32 v56, v211, v97
	ds_read_b128 v[94:97], v63 offset:768
	s_waitcnt lgkmcnt(2)
	v_fmac_f32_e32 v55, v204, v98
	v_fmac_f32_e32 v57, v208, v98
	v_fmac_f32_e32 v55, v205, v99
	v_fmac_f32_e32 v57, v209, v99
	v_fmac_f32_e32 v55, v206, v100
	v_fmac_f32_e32 v57, v210, v100
	v_fmac_f32_e32 v55, v207, v101
	v_fmac_f32_e32 v57, v211, v101
	ds_read_b128 v[98:101], v63 offset:1024
	s_waitcnt lgkmcnt(2)
	v_fmac_f32_e32 v50, v204, v58
	v_fmac_f32_e32 v52, v208, v58
	v_fmac_f32_e32 v50, v205, v59
	v_fmac_f32_e32 v52, v209, v59
	v_fmac_f32_e32 v50, v206, v60
	v_fmac_f32_e32 v52, v210, v60
	v_fmac_f32_e32 v50, v207, v61
	v_fmac_f32_e32 v52, v211, v61
	ds_read_b128 v[58:61], v63 offset:1280
	s_waitcnt lgkmcnt(2)
	v_fmac_f32_e32 v51, v204, v94
	v_fmac_f32_e32 v53, v208, v94
	v_fmac_f32_e32 v51, v205, v95
	v_fmac_f32_e32 v53, v209, v95
	v_fmac_f32_e32 v51, v206, v96
	v_fmac_f32_e32 v53, v210, v96
	v_fmac_f32_e32 v51, v207, v97
	v_fmac_f32_e32 v53, v211, v97
	ds_read_b128 v[94:97], v63 offset:1536
	s_waitcnt lgkmcnt(2)
	v_fmac_f32_e32 v46, v204, v98
	v_fmac_f32_e32 v48, v208, v98
	v_fmac_f32_e32 v46, v205, v99
	v_fmac_f32_e32 v48, v209, v99
	v_fmac_f32_e32 v46, v206, v100
	v_fmac_f32_e32 v48, v210, v100
	v_fmac_f32_e32 v46, v207, v101
	v_fmac_f32_e32 v48, v211, v101
	ds_read_b128 v[98:101], v63 offset:1792
	s_waitcnt lgkmcnt(2)
	v_fmac_f32_e32 v47, v204, v58
	v_fmac_f32_e32 v49, v208, v58
	v_fmac_f32_e32 v47, v205, v59
	v_fmac_f32_e32 v49, v209, v59
	v_fmac_f32_e32 v47, v206, v60
	v_fmac_f32_e32 v49, v210, v60
	v_fmac_f32_e32 v47, v207, v61
	v_fmac_f32_e32 v49, v211, v61
	ds_read_b128 v[58:61], v63 offset:2048
	s_waitcnt lgkmcnt(2)
	v_fmac_f32_e32 v42, v204, v94
	v_fmac_f32_e32 v44, v208, v94
	v_fmac_f32_e32 v42, v205, v95
	v_fmac_f32_e32 v44, v209, v95
	v_fmac_f32_e32 v42, v206, v96
	v_fmac_f32_e32 v44, v210, v96
	v_fmac_f32_e32 v42, v207, v97
	v_fmac_f32_e32 v44, v211, v97
	ds_read_b128 v[94:97], v63 offset:2304
	s_waitcnt lgkmcnt(2)
	v_fmac_f32_e32 v43, v204, v98
	v_fmac_f32_e32 v45, v208, v98
	v_fmac_f32_e32 v43, v205, v99
	v_fmac_f32_e32 v45, v209, v99
	v_fmac_f32_e32 v43, v206, v100
	v_fmac_f32_e32 v45, v210, v100
	v_fmac_f32_e32 v43, v207, v101
	v_fmac_f32_e32 v45, v211, v101
	ds_read_b128 v[98:101], v63 offset:2560
	s_waitcnt lgkmcnt(2)
	v_fmac_f32_e32 v38, v204, v58
	v_fmac_f32_e32 v40, v208, v58
	v_fmac_f32_e32 v38, v205, v59
	v_fmac_f32_e32 v40, v209, v59
	v_fmac_f32_e32 v38, v206, v60
	v_fmac_f32_e32 v40, v210, v60
	v_fmac_f32_e32 v38, v207, v61
	v_fmac_f32_e32 v40, v211, v61
	ds_read_b128 v[58:61], v63 offset:2816
	s_waitcnt lgkmcnt(2)
	v_fmac_f32_e32 v39, v204, v94
	v_fmac_f32_e32 v41, v208, v94
	v_fmac_f32_e32 v39, v205, v95
	v_fmac_f32_e32 v41, v209, v95
	v_fmac_f32_e32 v39, v206, v96
	v_fmac_f32_e32 v41, v210, v96
	v_fmac_f32_e32 v39, v207, v97
	v_fmac_f32_e32 v41, v211, v97
	ds_read_b128 v[94:97], v63 offset:3072
	s_waitcnt lgkmcnt(2)
;     ...
;         for (int k4 = 0; k4 < 16; ++k4) {
;             float wf[4], wb[4];
; #pragma unroll
;             for (int j = 0; j < 4; ++j) { wf[j] = w3[(k4 * 4 + j) * 1024 + tid]; wb[j] = w3[(k4 * 4 + j) * 1024 + 512 + tid]; }
; #pragma unroll
;             for (int pp = 0; pp < 16; ++pp) {
;                 const float4 hv = *(const float4*)&h2[(hp * 16 + pp) * 64 + k4 * 4];
;                 accf[pp] += hv.x * wf[0]; accf[pp] += hv.y * wf[1]; accf[pp] += hv.z * wf[2]; accf[pp] += hv.w * wf[3];
;                 accb[pp] += hv.x * wb[0]; accb[pp] += hv.y * wb[1]; accb[pp] += hv.z * wb[2]; accb[pp] += hv.w * wb[3];
;             }
;         }
	v_fmac_f32_e32 v34, v204, v98
	v_fmac_f32_e32 v36, v208, v98
	v_fmac_f32_e32 v34, v205, v99
	v_fmac_f32_e32 v36, v209, v99
	v_fmac_f32_e32 v34, v206, v100
	v_fmac_f32_e32 v36, v210, v100
	v_fmac_f32_e32 v34, v207, v101
	v_fmac_f32_e32 v36, v211, v101
	ds_read_b128 v[98:101], v63 offset:3328
	s_waitcnt lgkmcnt(2)
	v_fmac_f32_e32 v35, v204, v58
	v_fmac_f32_e32 v37, v208, v58
	v_fmac_f32_e32 v35, v205, v59
	v_fmac_f32_e32 v37, v209, v59
	v_fmac_f32_e32 v35, v206, v60
	v_fmac_f32_e32 v37, v210, v60
	v_fmac_f32_e32 v35, v207, v61
	v_fmac_f32_e32 v37, v211, v61
	ds_read_b128 v[58:61], v63 offset:3584
	s_waitcnt lgkmcnt(2)
	v_fmac_f32_e32 v30, v204, v94
	v_fmac_f32_e32 v32, v208, v94
	v_fmac_f32_e32 v30, v205, v95
	v_fmac_f32_e32 v32, v209, v95
	v_fmac_f32_e32 v30, v206, v96
	v_fmac_f32_e32 v32, v210, v96
	v_fmac_f32_e32 v30, v207, v97
	v_fmac_f32_e32 v32, v211, v97
	ds_read_b128 v[94:97], v63 offset:3840
	s_waitcnt lgkmcnt(2)
	v_fmac_f32_e32 v31, v204, v98
	v_fmac_f32_e32 v33, v208, v98
	v_fmac_f32_e32 v31, v205, v99
	v_fmac_f32_e32 v33, v209, v99
	v_fmac_f32_e32 v31, v206, v100
	v_fmac_f32_e32 v33, v210, v100
	v_fmac_f32_e32 v31, v207, v101
	v_fmac_f32_e32 v33, v211, v101
	s_waitcnt lgkmcnt(1)
	v_fmac_f32_e32 v26, v204, v58
	v_fmac_f32_e32 v28, v208, v58
	v_fmac_f32_e32 v26, v205, v59
	v_fmac_f32_e32 v28, v209, v59
	v_fmac_f32_e32 v26, v206, v60
	v_fmac_f32_e32 v28, v210, v60
	v_fmac_f32_e32 v26, v207, v61
	v_fmac_f32_e32 v28, v211, v61
	s_waitcnt lgkmcnt(0)
	v_fmac_f32_e32 v27, v204, v94
	v_fmac_f32_e32 v29, v208, v94
	v_fmac_f32_e32 v27, v205, v95
	v_fmac_f32_e32 v29, v209, v95
	v_fmac_f32_e32 v27, v206, v96
	v_fmac_f32_e32 v29, v210, v96
	v_fmac_f32_e32 v27, v207, v97
	v_fmac_f32_e32 v29, v211, v97
	v_mov_b32_e32 v63, s101
	s_add_i32 s101, s101, 16
	ds_read_b128 v[94:97], v63
	ds_read_b128 v[98:101], v63 offset:256
	s_waitcnt vmcnt(16)
	ds_read_b128 v[58:61], v63 offset:512
	s_waitcnt lgkmcnt(2)
	v_fmac_f32_e32 v54, v212, v94
	v_fmac_f32_e32 v56, v216, v94
	v_fmac_f32_e32 v54, v213, v95
	v_fmac_f32_e32 v56, v217, v95
	v_fmac_f32_e32 v54, v214, v96
	v_fmac_f32_e32 v56, v218, v96
	v_fmac_f32_e32 v54, v215, v97
	v_fmac_f32_e32 v56, v219, v97
	ds_read_b128 v[94:97], v63 offset:768
	s_waitcnt lgkmcnt(2)
	v_fmac_f32_e32 v55, v212, v98
	v_fmac_f32_e32 v57, v216, v98
	v_fmac_f32_e32 v55, v213, v99
	v_fmac_f32_e32 v57, v217, v99
	v_fmac_f32_e32 v55, v214, v100
	v_fmac_f32_e32 v57, v218, v100
	v_fmac_f32_e32 v55, v215, v101
	v_fmac_f32_e32 v57, v219, v101
	ds_read_b128 v[98:101], v63 offset:1024
	s_waitcnt lgkmcnt(2)
	v_fmac_f32_e32 v50, v212, v58
	v_fmac_f32_e32 v52, v216, v58
	v_fmac_f32_e32 v50, v213, v59
	v_fmac_f32_e32 v52, v217, v59
	v_fmac_f32_e32 v50, v214, v60
	v_fmac_f32_e32 v52, v218, v60
	v_fmac_f32_e32 v50, v215, v61
	v_fmac_f32_e32 v52, v219, v61
	ds_read_b128 v[58:61], v63 offset:1280
	s_waitcnt lgkmcnt(2)
	v_fmac_f32_e32 v51, v212, v94
	v_fmac_f32_e32 v53, v216, v94
	v_fmac_f32_e32 v51, v213, v95
	v_fmac_f32_e32 v53, v217, v95
	v_fmac_f32_e32 v51, v214, v96
	v_fmac_f32_e32 v53, v218, v96
	v_fmac_f32_e32 v51, v215, v97
	v_fmac_f32_e32 v53, v219, v97
	ds_read_b128 v[94:97], v63 offset:1536
	s_waitcnt lgkmcnt(2)
	v_fmac_f32_e32 v46, v212, v98
	v_fmac_f32_e32 v48, v216, v98
	v_fmac_f32_e32 v46, v213, v99
	v_fmac_f32_e32 v48, v217, v99
	v_fmac_f32_e32 v46, v214, v100
	v_fmac_f32_e32 v48, v218, v100
	v_fmac_f32_e32 v46, v215, v101
	v_fmac_f32_e32 v48, v219, v101
	ds_read_b128 v[98:101], v63 offset:1792
	s_waitcnt lgkmcnt(2)
	v_fmac_f32_e32 v47, v212, v58
	v_fmac_f32_e32 v49, v216, v58
	v_fmac_f32_e32 v47, v213, v59
	v_fmac_f32_e32 v49, v217, v59
	v_fmac_f32_e32 v47, v214, v60
	v_fmac_f32_e32 v49, v218, v60
	v_fmac_f32_e32 v47, v215, v61
	v_fmac_f32_e32 v49, v219, v61
	ds_read_b128 v[58:61], v63 offset:2048
	s_waitcnt lgkmcnt(2)
	v_fmac_f32_e32 v42, v212, v94
	v_fmac_f32_e32 v44, v216, v94
	v_fmac_f32_e32 v42, v213, v95
	v_fmac_f32_e32 v44, v217, v95
	v_fmac_f32_e32 v42, v214, v96
	v_fmac_f32_e32 v44, v218, v96
	v_fmac_f32_e32 v42, v215, v97
	v_fmac_f32_e32 v44, v219, v97
	ds_read_b128 v[94:97], v63 offset:2304
	s_waitcnt lgkmcnt(2)
	v_fmac_f32_e32 v43, v212, v98
	v_fmac_f32_e32 v45, v216, v98
	v_fmac_f32_e32 v43, v213, v99
	v_fmac_f32_e32 v45, v217, v99
	v_fmac_f32_e32 v43, v214, v100
	v_fmac_f32_e32 v45, v218, v100
	v_fmac_f32_e32 v43, v215, v101
	v_fmac_f32_e32 v45, v219, v101
	ds_read_b128 v[98:101], v63 offset:2560
	s_waitcnt lgkmcnt(2)
	v_fmac_f32_e32 v38, v212, v58
	v_fmac_f32_e32 v40, v216, v58
	v_fmac_f32_e32 v38, v213, v59
	v_fmac_f32_e32 v40, v217, v59
	v_fmac_f32_e32 v38, v214, v60
	v_fmac_f32_e32 v40, v218, v60
	v_fmac_f32_e32 v38, v215, v61
	v_fmac_f32_e32 v40, v219, v61
	ds_read_b128 v[58:61], v63 offset:2816
	s_waitcnt lgkmcnt(2)
	v_fmac_f32_e32 v39, v212, v94
	v_fmac_f32_e32 v41, v216, v94
	v_fmac_f32_e32 v39, v213, v95
	v_fmac_f32_e32 v41, v217, v95
	v_fmac_f32_e32 v39, v214, v96
	v_fmac_f32_e32 v41, v218, v96
	v_fmac_f32_e32 v39, v215, v97
	v_fmac_f32_e32 v41, v219, v97
	ds_read_b128 v[94:97], v63 offset:3072
	s_waitcnt lgkmcnt(2)
	v_fmac_f32_e32 v34, v212, v98
	v_fmac_f32_e32 v36, v216, v98
	v_fmac_f32_e32 v34, v213, v99
	v_fmac_f32_e32 v36, v217, v99
	v_fmac_f32_e32 v34, v214, v100
	v_fmac_f32_e32 v36, v218, v100
	v_fmac_f32_e32 v34, v215, v101
	v_fmac_f32_e32 v36, v219, v101
	ds_read_b128 v[98:101], v63 offset:3328
	s_waitcnt lgkmcnt(2)
	v_fmac_f32_e32 v35, v212, v58
	v_fmac_f32_e32 v37, v216, v58
	v_fmac_f32_e32 v35, v213, v59
	v_fmac_f32_e32 v37, v217, v59
	v_fmac_f32_e32 v35, v214, v60
	v_fmac_f32_e32 v37, v218, v60
	v_fmac_f32_e32 v35, v215, v61
	v_fmac_f32_e32 v37, v219, v61
	ds_read_b128 v[58:61], v63 offset:3584
	s_waitcnt lgkmcnt(2)
;     ...
;         for (int k4 = 0; k4 < 16; ++k4) {
;             float wf[4], wb[4];
; #pragma unroll
;             for (int j = 0; j < 4; ++j) { wf[j] = w3[(k4 * 4 + j) * 1024 + tid]; wb[j] = w3[(k4 * 4 + j) * 1024 + 512 + tid]; }
; #pragma unroll
;             for (int pp = 0; pp < 16; ++pp) {
;                 const float4 hv = *(const float4*)&h2[(hp * 16 + pp) * 64 + k4 * 4];
;                 accf[pp] += hv.x * wf[0]; accf[pp] += hv.y * wf[1]; accf[pp] += hv.z * wf[2]; accf[pp] += hv.w * wf[3];
;                 accb[pp] += hv.x * wb[0]; accb[pp] += hv.y * wb[1]; accb[pp] += hv.z * wb[2]; accb[pp] += hv.w * wb[3];
;             }
;         }
	v_fmac_f32_e32 v30, v212, v94
	v_fmac_f32_e32 v32, v216, v94
	v_fmac_f32_e32 v30, v213, v95
	v_fmac_f32_e32 v32, v217, v95
	v_fmac_f32_e32 v30, v214, v96
	v_fmac_f32_e32 v32, v218, v96
	v_fmac_f32_e32 v30, v215, v97
	v_fmac_f32_e32 v32, v219, v97
	ds_read_b128 v[94:97], v63 offset:3840
	s_waitcnt lgkmcnt(2)
	v_fmac_f32_e32 v31, v212, v98
	v_fmac_f32_e32 v33, v216, v98
	v_fmac_f32_e32 v31, v213, v99
	v_fmac_f32_e32 v33, v217, v99
	v_fmac_f32_e32 v31, v214, v100
	v_fmac_f32_e32 v33, v218, v100
	v_fmac_f32_e32 v31, v215, v101
	v_fmac_f32_e32 v33, v219, v101
	s_waitcnt lgkmcnt(1)
	v_fmac_f32_e32 v26, v212, v58
	v_fmac_f32_e32 v28, v216, v58
	v_fmac_f32_e32 v26, v213, v59
	v_fmac_f32_e32 v28, v217, v59
	v_fmac_f32_e32 v26, v214, v60
	v_fmac_f32_e32 v28, v218, v60
	v_fmac_f32_e32 v26, v215, v61
	v_fmac_f32_e32 v28, v219, v61
	s_waitcnt lgkmcnt(0)
	v_fmac_f32_e32 v27, v212, v94
	v_fmac_f32_e32 v29, v216, v94
	v_fmac_f32_e32 v27, v213, v95
	v_fmac_f32_e32 v29, v217, v95
	v_fmac_f32_e32 v27, v214, v96
	v_fmac_f32_e32 v29, v218, v96
	v_fmac_f32_e32 v27, v215, v97
	v_fmac_f32_e32 v29, v219, v97
	v_mov_b32_e32 v63, s101
	s_add_i32 s101, s101, 16
	ds_read_b128 v[94:97], v63
	ds_read_b128 v[98:101], v63 offset:256
	s_waitcnt vmcnt(8)
	ds_read_b128 v[58:61], v63 offset:512
	s_waitcnt lgkmcnt(2)
	v_fmac_f32_e32 v54, v220, v94
	v_fmac_f32_e32 v56, v224, v94
	v_fmac_f32_e32 v54, v221, v95
	v_fmac_f32_e32 v56, v225, v95
	v_fmac_f32_e32 v54, v222, v96
	v_fmac_f32_e32 v56, v226, v96
	v_fmac_f32_e32 v54, v223, v97
	v_fmac_f32_e32 v56, v227, v97
	ds_read_b128 v[94:97], v63 offset:768
	s_waitcnt lgkmcnt(2)
	v_fmac_f32_e32 v55, v220, v98
	v_fmac_f32_e32 v57, v224, v98
	v_fmac_f32_e32 v55, v221, v99
	v_fmac_f32_e32 v57, v225, v99
	v_fmac_f32_e32 v55, v222, v100
	v_fmac_f32_e32 v57, v226, v100
	v_fmac_f32_e32 v55, v223, v101
	v_fmac_f32_e32 v57, v227, v101
	ds_read_b128 v[98:101], v63 offset:1024
	s_waitcnt lgkmcnt(2)
	v_fmac_f32_e32 v50, v220, v58
	v_fmac_f32_e32 v52, v224, v58
	v_fmac_f32_e32 v50, v221, v59
	v_fmac_f32_e32 v52, v225, v59
	v_fmac_f32_e32 v50, v222, v60
	v_fmac_f32_e32 v52, v226, v60
	v_fmac_f32_e32 v50, v223, v61
	v_fmac_f32_e32 v52, v227, v61
	ds_read_b128 v[58:61], v63 offset:1280
	s_waitcnt lgkmcnt(2)
	v_fmac_f32_e32 v51, v220, v94
	v_fmac_f32_e32 v53, v224, v94
	v_fmac_f32_e32 v51, v221, v95
	v_fmac_f32_e32 v53, v225, v95
	v_fmac_f32_e32 v51, v222, v96
	v_fmac_f32_e32 v53, v226, v96
	v_fmac_f32_e32 v51, v223, v97
	v_fmac_f32_e32 v53, v227, v97
	ds_read_b128 v[94:97], v63 offset:1536
	s_waitcnt lgkmcnt(2)
	v_fmac_f32_e32 v46, v220, v98
	v_fmac_f32_e32 v48, v224, v98
	v_fmac_f32_e32 v46, v221, v99
	v_fmac_f32_e32 v48, v225, v99
	v_fmac_f32_e32 v46, v222, v100
	v_fmac_f32_e32 v48, v226, v100
	v_fmac_f32_e32 v46, v223, v101
	v_fmac_f32_e32 v48, v227, v101
	ds_read_b128 v[98:101], v63 offset:1792
	s_waitcnt lgkmcnt(2)
	v_fmac_f32_e32 v47, v220, v58
	v_fmac_f32_e32 v49, v224, v58
	v_fmac_f32_e32 v47, v221, v59
	v_fmac_f32_e32 v49, v225, v59
	v_fmac_f32_e32 v47, v222, v60
	v_fmac_f32_e32 v49, v226, v60
	v_fmac_f32_e32 v47, v223, v61
	v_fmac_f32_e32 v49, v227, v61
	ds_read_b128 v[58:61], v63 offset:2048
	s_waitcnt lgkmcnt(2)
	v_fmac_f32_e32 v42, v220, v94
	v_fmac_f32_e32 v44, v224, v94
	v_fmac_f32_e32 v42, v221, v95
	v_fmac_f32_e32 v44, v225, v95
	v_fmac_f32_e32 v42, v222, v96
	v_fmac_f32_e32 v44, v226, v96
	v_fmac_f32_e32 v42, v223, v97
	v_fmac_f32_e32 v44, v227, v97
	ds_read_b128 v[94:97], v63 offset:2304
	s_waitcnt lgkmcnt(2)
	v_fmac_f32_e32 v43, v220, v98
	v_fmac_f32_e32 v45, v224, v98
	v_fmac_f32_e32 v43, v221, v99
	v_fmac_f32_e32 v45, v225, v99
	v_fmac_f32_e32 v43, v222, v100
	v_fmac_f32_e32 v45, v226, v100
	v_fmac_f32_e32 v43, v223, v101
	v_fmac_f32_e32 v45, v227, v101
	ds_read_b128 v[98:101], v63 offset:2560
	s_waitcnt lgkmcnt(2)
	v_fmac_f32_e32 v38, v220, v58
	v_fmac_f32_e32 v40, v224, v58
	v_fmac_f32_e32 v38, v221, v59
	v_fmac_f32_e32 v40, v225, v59
	v_fmac_f32_e32 v38, v222, v60
	v_fmac_f32_e32 v40, v226, v60
	v_fmac_f32_e32 v38, v223, v61
	v_fmac_f32_e32 v40, v227, v61
	ds_read_b128 v[58:61], v63 offset:2816
	s_waitcnt lgkmcnt(2)
	v_fmac_f32_e32 v39, v220, v94
	v_fmac_f32_e32 v41, v224, v94
	v_fmac_f32_e32 v39, v221, v95
	v_fmac_f32_e32 v41, v225, v95
	v_fmac_f32_e32 v39, v222, v96
	v_fmac_f32_e32 v41, v226, v96
	v_fmac_f32_e32 v39, v223, v97
	v_fmac_f32_e32 v41, v227, v97
	ds_read_b128 v[94:97], v63 offset:3072
	s_waitcnt lgkmcnt(2)
	v_fmac_f32_e32 v34, v220, v98
	v_fmac_f32_e32 v36, v224, v98
	v_fmac_f32_e32 v34, v221, v99
	v_fmac_f32_e32 v36, v225, v99
	v_fmac_f32_e32 v34, v222, v100
	v_fmac_f32_e32 v36, v226, v100
	v_fmac_f32_e32 v34, v223, v101
	v_fmac_f32_e32 v36, v227, v101
	ds_read_b128 v[98:101], v63 offset:3328
	s_waitcnt lgkmcnt(2)
	v_fmac_f32_e32 v35, v220, v58
	v_fmac_f32_e32 v37, v224, v58
	v_fmac_f32_e32 v35, v221, v59
	v_fmac_f32_e32 v37, v225, v59
	v_fmac_f32_e32 v35, v222, v60
	v_fmac_f32_e32 v37, v226, v60
	v_fmac_f32_e32 v35, v223, v61
	v_fmac_f32_e32 v37, v227, v61
	ds_read_b128 v[58:61], v63 offset:3584
	s_waitcnt lgkmcnt(2)
	v_fmac_f32_e32 v30, v220, v94
	v_fmac_f32_e32 v32, v224, v94
	v_fmac_f32_e32 v30, v221, v95
	v_fmac_f32_e32 v32, v225, v95
	v_fmac_f32_e32 v30, v222, v96
	v_fmac_f32_e32 v32, v226, v96
	v_fmac_f32_e32 v30, v223, v97
	v_fmac_f32_e32 v32, v227, v97
	ds_read_b128 v[94:97], v63 offset:3840
	s_waitcnt lgkmcnt(2)
	v_fmac_f32_e32 v31, v220, v98
	v_fmac_f32_e32 v33, v224, v98
	v_fmac_f32_e32 v31, v221, v99
	v_fmac_f32_e32 v33, v225, v99
	v_fmac_f32_e32 v31, v222, v100
	v_fmac_f32_e32 v33, v226, v100
	v_fmac_f32_e32 v31, v223, v101
	v_fmac_f32_e32 v33, v227, v101
	s_waitcnt lgkmcnt(1)
;     ...
;         for (int k4 = 0; k4 < 16; ++k4) {
;             float wf[4], wb[4];
; #pragma unroll
;             for (int j = 0; j < 4; ++j) { wf[j] = w3[(k4 * 4 + j) * 1024 + tid]; wb[j] = w3[(k4 * 4 + j) * 1024 + 512 + tid]; }
; #pragma unroll
;             for (int pp = 0; pp < 16; ++pp) {
;                 const float4 hv = *(const float4*)&h2[(hp * 16 + pp) * 64 + k4 * 4];
;                 accf[pp] += hv.x * wf[0]; accf[pp] += hv.y * wf[1]; accf[pp] += hv.z * wf[2]; accf[pp] += hv.w * wf[3];
;                 accb[pp] += hv.x * wb[0]; accb[pp] += hv.y * wb[1]; accb[pp] += hv.z * wb[2]; accb[pp] += hv.w * wb[3];
;             }
;         }
; #pragma unroll
;         for (int pp = 0; pp < 16; ++pp) {
;             const int pos = p0 + hp * 16 + pp;
;             const float t = (float)pos / (float)(l - 1);
;             const float win = expf(-t * delta);
;             const float f = accf[pp] * win, b = accb[pp] * win;
;             HF[pos] = f; asum += fabsf(f);
;             if (pos >= 1) { HF[-pos] = b; asum += fabsf(b); }
	v_fmac_f32_e32 v26, v220, v58
	v_fmac_f32_e32 v28, v224, v58
	v_fmac_f32_e32 v26, v221, v59
	v_fmac_f32_e32 v28, v225, v59
	v_fmac_f32_e32 v26, v222, v60
	v_fmac_f32_e32 v28, v226, v60
	v_fmac_f32_e32 v26, v223, v61
	v_fmac_f32_e32 v28, v227, v61
	s_waitcnt lgkmcnt(0)
	v_fmac_f32_e32 v27, v220, v94
	v_fmac_f32_e32 v29, v224, v94
	v_fmac_f32_e32 v27, v221, v95
	v_fmac_f32_e32 v29, v225, v95
	v_fmac_f32_e32 v27, v222, v96
	v_fmac_f32_e32 v29, v226, v96
	v_fmac_f32_e32 v27, v223, v97
	v_fmac_f32_e32 v29, v227, v97
	v_mov_b32_e32 v63, s101
	s_add_i32 s101, s101, 16
	ds_read_b128 v[94:97], v63
	ds_read_b128 v[98:101], v63 offset:256
	s_waitcnt vmcnt(0)
	ds_read_b128 v[58:61], v63 offset:512
	s_waitcnt lgkmcnt(2)
	v_fmac_f32_e32 v54, v228, v94
	v_fmac_f32_e32 v56, v232, v94
	v_fmac_f32_e32 v54, v229, v95
	v_fmac_f32_e32 v56, v233, v95
	v_fmac_f32_e32 v54, v230, v96
	v_fmac_f32_e32 v56, v234, v96
	v_fmac_f32_e32 v54, v231, v97
	v_fmac_f32_e32 v56, v235, v97
	ds_read_b128 v[94:97], v63 offset:768
	s_waitcnt lgkmcnt(2)
	v_fmac_f32_e32 v55, v228, v98
	v_fmac_f32_e32 v57, v232, v98
	v_fmac_f32_e32 v55, v229, v99
	v_fmac_f32_e32 v57, v233, v99
	v_fmac_f32_e32 v55, v230, v100
	v_fmac_f32_e32 v57, v234, v100
	v_fmac_f32_e32 v55, v231, v101
	v_fmac_f32_e32 v57, v235, v101
	ds_read_b128 v[98:101], v63 offset:1024
	s_waitcnt lgkmcnt(2)
	v_fmac_f32_e32 v50, v228, v58
	v_fmac_f32_e32 v52, v232, v58
	v_fmac_f32_e32 v50, v229, v59
	v_fmac_f32_e32 v52, v233, v59
	v_fmac_f32_e32 v50, v230, v60
	v_fmac_f32_e32 v52, v234, v60
	v_fmac_f32_e32 v50, v231, v61
	v_fmac_f32_e32 v52, v235, v61
	ds_read_b128 v[58:61], v63 offset:1280
	s_waitcnt lgkmcnt(2)
	v_fmac_f32_e32 v51, v228, v94
	v_fmac_f32_e32 v53, v232, v94
	v_fmac_f32_e32 v51, v229, v95
	v_fmac_f32_e32 v53, v233, v95
	v_fmac_f32_e32 v51, v230, v96
	v_fmac_f32_e32 v53, v234, v96
	v_fmac_f32_e32 v51, v231, v97
	v_fmac_f32_e32 v53, v235, v97
	ds_read_b128 v[94:97], v63 offset:1536
	s_waitcnt lgkmcnt(2)
	v_fmac_f32_e32 v46, v228, v98
	v_fmac_f32_e32 v48, v232, v98
	v_fmac_f32_e32 v46, v229, v99
	v_fmac_f32_e32 v48, v233, v99
	v_fmac_f32_e32 v46, v230, v100
	v_fmac_f32_e32 v48, v234, v100
	v_fmac_f32_e32 v46, v231, v101
	v_fmac_f32_e32 v48, v235, v101
	ds_read_b128 v[98:101], v63 offset:1792
	s_waitcnt lgkmcnt(2)
	v_fmac_f32_e32 v47, v228, v58
	v_fmac_f32_e32 v49, v232, v58
	v_fmac_f32_e32 v47, v229, v59
	v_fmac_f32_e32 v49, v233, v59
	v_fmac_f32_e32 v47, v230, v60
	v_fmac_f32_e32 v49, v234, v60
	v_fmac_f32_e32 v47, v231, v61
	v_fmac_f32_e32 v49, v235, v61
	ds_read_b128 v[58:61], v63 offset:2048
	s_waitcnt lgkmcnt(2)
	v_fmac_f32_e32 v42, v228, v94
	v_fmac_f32_e32 v44, v232, v94
	v_fmac_f32_e32 v42, v229, v95
	v_fmac_f32_e32 v44, v233, v95
	v_fmac_f32_e32 v42, v230, v96
	v_fmac_f32_e32 v44, v234, v96
	v_fmac_f32_e32 v42, v231, v97
	v_fmac_f32_e32 v44, v235, v97
	ds_read_b128 v[94:97], v63 offset:2304
	s_waitcnt lgkmcnt(2)
	v_fmac_f32_e32 v43, v228, v98
	v_fmac_f32_e32 v45, v232, v98
	v_fmac_f32_e32 v43, v229, v99
	v_fmac_f32_e32 v45, v233, v99
	v_fmac_f32_e32 v43, v230, v100
	v_fmac_f32_e32 v45, v234, v100
	v_fmac_f32_e32 v43, v231, v101
	v_fmac_f32_e32 v45, v235, v101
	ds_read_b128 v[98:101], v63 offset:2560
	s_waitcnt lgkmcnt(2)
	v_fmac_f32_e32 v38, v228, v58
	v_fmac_f32_e32 v40, v232, v58
	v_fmac_f32_e32 v38, v229, v59
	v_fmac_f32_e32 v40, v233, v59
	v_fmac_f32_e32 v38, v230, v60
	v_fmac_f32_e32 v40, v234, v60
	v_fmac_f32_e32 v38, v231, v61
	v_fmac_f32_e32 v40, v235, v61
	ds_read_b128 v[58:61], v63 offset:2816
	s_waitcnt lgkmcnt(2)
	v_fmac_f32_e32 v39, v228, v94
	v_fmac_f32_e32 v41, v232, v94
	v_fmac_f32_e32 v39, v229, v95
	v_fmac_f32_e32 v41, v233, v95
	v_fmac_f32_e32 v39, v230, v96
	v_fmac_f32_e32 v41, v234, v96
	v_fmac_f32_e32 v39, v231, v97
	v_fmac_f32_e32 v41, v235, v97
	ds_read_b128 v[94:97], v63 offset:3072
	s_waitcnt lgkmcnt(2)
	v_fmac_f32_e32 v34, v228, v98
	v_fmac_f32_e32 v36, v232, v98
	v_fmac_f32_e32 v34, v229, v99
	v_fmac_f32_e32 v36, v233, v99
	v_fmac_f32_e32 v34, v230, v100
	v_fmac_f32_e32 v36, v234, v100
	v_fmac_f32_e32 v34, v231, v101
	v_fmac_f32_e32 v36, v235, v101
	ds_read_b128 v[98:101], v63 offset:3328
	s_waitcnt lgkmcnt(2)
	v_fmac_f32_e32 v35, v228, v58
	v_fmac_f32_e32 v37, v232, v58
	v_fmac_f32_e32 v35, v229, v59
	v_fmac_f32_e32 v37, v233, v59
	v_fmac_f32_e32 v35, v230, v60
	v_fmac_f32_e32 v37, v234, v60
	v_fmac_f32_e32 v35, v231, v61
	v_fmac_f32_e32 v37, v235, v61
	ds_read_b128 v[58:61], v63 offset:3584
	s_waitcnt lgkmcnt(2)
	v_fmac_f32_e32 v30, v228, v94
	v_fmac_f32_e32 v32, v232, v94
	v_fmac_f32_e32 v30, v229, v95
	v_fmac_f32_e32 v32, v233, v95
	v_fmac_f32_e32 v30, v230, v96
	v_fmac_f32_e32 v32, v234, v96
	v_fmac_f32_e32 v30, v231, v97
	v_fmac_f32_e32 v32, v235, v97
	ds_read_b128 v[94:97], v63 offset:3840
	s_waitcnt lgkmcnt(2)
	v_fmac_f32_e32 v31, v228, v98
	v_fmac_f32_e32 v33, v232, v98
	v_fmac_f32_e32 v31, v229, v99
	v_fmac_f32_e32 v33, v233, v99
	v_fmac_f32_e32 v31, v230, v100
	v_fmac_f32_e32 v33, v234, v100
	v_fmac_f32_e32 v31, v231, v101
	v_fmac_f32_e32 v33, v235, v101
	s_waitcnt lgkmcnt(1)
	v_fmac_f32_e32 v26, v228, v58
	v_fmac_f32_e32 v28, v232, v58
	v_fmac_f32_e32 v26, v229, v59
	v_fmac_f32_e32 v28, v233, v59
	v_fmac_f32_e32 v26, v230, v60
	v_fmac_f32_e32 v28, v234, v60
	v_fmac_f32_e32 v26, v231, v61
	v_fmac_f32_e32 v28, v235, v61
	s_waitcnt lgkmcnt(0)
	v_fmac_f32_e32 v27, v228, v94
	v_fmac_f32_e32 v29, v232, v94
	v_fmac_f32_e32 v27, v229, v95
	v_fmac_f32_e32 v29, v233, v95
	v_fmac_f32_e32 v27, v230, v96
	v_fmac_f32_e32 v29, v234, v96
	v_fmac_f32_e32 v27, v231, v97
	v_fmac_f32_e32 v29, v235, v97
	v_lshrrev_b32_e32 v78, 6, v0
	v_and_b32_e32 v79, 63, v0
	v_mul_u32_u24_e32 v78, 0x2100, v78
	v_mul_u32_u24_e32 v79, 0x84, v79
	v_add_u32_e32 v78, v78, v79
	v_add_u32_e32 v78, 0xa000, v78
	s_lshl_b32 s2, s7, 4
	s_or_b32 s2, s2, s15
	v_cvt_f32_i32_e32 v2, s2
	s_ashr_i32 s3, s2, 31
	s_cmp_gt_i32 s2, 0
	v_div_scale_f32 v3, s[4:5], v77, v77, -v2
	v_rcp_f32_e32 v4, v3
	v_div_scale_f32 v5, vcc, -v2, v77, -v2
	v_fma_f32 v58, -v3, v4, 1.0
	v_fmac_f32_e32 v4, v58, v4
	v_mul_f32_e32 v58, v5, v4
	v_fma_f32 v59, -v3, v58, v5
	v_fmac_f32_e32 v58, v59, v4
	v_fma_f32 v3, -v3, v58, v5
	v_div_fmas_f32 v3, v3, v4, v58
	v_div_fixup_f32 v2, v3, v77, -v2
	v_mul_f32_e64 v2, |v67|, v2
	v_mul_f32_e32 v3, 0x3fb8aa3b, v2
	v_fma_f32 v4, v2, s40, -v3
	v_rndne_f32_e32 v5, v3
	v_fmac_f32_e32 v4, 0x32a5705f, v2
	v_sub_f32_e32 v3, v3, v5
	v_add_f32_e32 v3, v3, v4
	v_cvt_i32_f32_e32 v4, v5
	v_exp_f32_e32 v3, v3
	v_cmp_ngt_f32_e32 vcc, s41, v2
	v_ldexp_f32 v3, v3, v4
	s_nop 0
	v_cndmask_b32_e32 v3, 0, v3, vcc
	v_cmp_nlt_f32_e32 vcc, s42, v2
	s_nop 1
	v_cndmask_b32_e32 v5, v76, v3, vcc
	v_mul_f32_e32 v4, v5, v54
	v_lshl_add_u64 v[2:3], s[2:3], 2, v[24:25]
	ds_write_b32 v78, v4 offset:0
	v_add_f32_e64 v4, v22, |v4|
	s_cbranch_scc0 .LBB0_79
	s_sub_i32 s4, 0, s2
	v_mul_f32_e32 v5, v5, v56
	s_ashr_i32 s5, s4, 31
	v_add_f32_e64 v4, |v5|, v4
	v_lshl_add_u64 v[58:59], s[4:5], 2, v[24:25]
	ds_write_b32 v78, v5 offset:124
